# lever 9 (sec 7.11): all 8 GEMM main loops - counter / pointer bump / exit test moved above the loop-back barrier so nothing but the branch sits between its release and the next ds_reads
# speedup vs baseline: 1.0011x; 1.0011x over previous
.LBB0_227:
	ds_read_b128 v[130:133], v159
	ds_read_b128 v[134:137], v159 offset:1024
	ds_read_b128 v[162:165], v159 offset:2048
	ds_read_b128 v[166:169], v159 offset:3072
	ds_read_b128 v[170:173], v160
	ds_read_b128 v[174:177], v160 offset:1024
	ds_read_b128 v[178:181], v160 offset:2048
	ds_read_b128 v[182:185], v160 offset:3072
	s_add_u32 s2, s34, 0xfff80080
	s_addc_u32 s3, s35, -1
	s_cmp_eq_u32 s56, 28
	s_cselect_b32 s39, s19, s3
	s_cselect_b32 s38, s29, s2
	s_cselect_b32 s37, s21, s55
	s_cselect_b32 s36, s31, s54
	v_lshl_add_u64 v[138:139], s[34:35], 0, v[152:153]
	s_add_i32 m0, s44, 0xc000
	ds_read_b128 v[186:189], v161
	ds_read_b128 v[190:193], v161 offset:1024
	ds_read_b128 v[194:197], v161 offset:2048
	ds_read_b128 v[198:201], v161 offset:3072
	ds_read_b128 v[202:205], v161 offset:4096
	ds_read_b128 v[206:209], v161 offset:5120
	ds_read_b128 v[210:213], v161 offset:6144
	ds_read_b128 v[214:217], v161 offset:7168
	global_load_lds_dwordx4 v[138:139], off
	v_lshl_add_u64 v[138:139], s[34:35], 0, v[150:151]
	s_add_i32 m0, s44, 0xe000
	s_nop 0
	global_load_lds_dwordx4 v[138:139], off
	s_waitcnt vmcnt(8)
	s_waitcnt lgkmcnt(0)
	s_barrier
	s_setprio 1
	s_waitcnt lgkmcnt(0)
	v_mfma_f32_16x16x32_bf16 v[126:129], v[130:133], v[186:189], v[126:129]
	v_mfma_f32_16x16x32_bf16 v[122:125], v[162:165], v[186:189], v[122:125]
	v_mfma_f32_16x16x32_bf16 v[110:113], v[130:133], v[194:197], v[110:113]
	v_mfma_f32_16x16x32_bf16 v[106:109], v[162:165], v[194:197], v[106:109]
	v_mfma_f32_16x16x32_bf16 v[94:97], v[130:133], v[202:205], v[94:97]
	v_mfma_f32_16x16x32_bf16 v[90:93], v[162:165], v[202:205], v[90:93]
	v_mfma_f32_16x16x32_bf16 v[78:81], v[130:133], v[210:213], v[78:81]
	v_mfma_f32_16x16x32_bf16 v[74:77], v[162:165], v[210:213], v[74:77]
	v_mfma_f32_16x16x32_bf16 v[126:129], v[134:137], v[190:193], v[126:129]
	v_mfma_f32_16x16x32_bf16 v[122:125], v[166:169], v[190:193], v[122:125]
	v_mfma_f32_16x16x32_bf16 v[110:113], v[134:137], v[198:201], v[110:113]
	v_mfma_f32_16x16x32_bf16 v[106:109], v[166:169], v[198:201], v[106:109]
	v_mfma_f32_16x16x32_bf16 v[94:97], v[134:137], v[206:209], v[94:97]
	v_mfma_f32_16x16x32_bf16 v[90:93], v[166:169], v[206:209], v[90:93]
	v_mfma_f32_16x16x32_bf16 v[78:81], v[134:137], v[214:217], v[78:81]
	v_mfma_f32_16x16x32_bf16 v[74:77], v[166:169], v[214:217], v[74:77]
	s_setprio 0
	s_setprio 1
	v_mfma_f32_16x16x32_bf16 v[118:121], v[170:173], v[186:189], v[118:121]
	v_mfma_f32_16x16x32_bf16 v[114:117], v[178:181], v[186:189], v[114:117]
	v_mfma_f32_16x16x32_bf16 v[102:105], v[170:173], v[194:197], v[102:105]
	v_mfma_f32_16x16x32_bf16 v[98:101], v[178:181], v[194:197], v[98:101]
	v_mfma_f32_16x16x32_bf16 v[86:89], v[170:173], v[202:205], v[86:89]
	v_mfma_f32_16x16x32_bf16 v[82:85], v[178:181], v[202:205], v[82:85]
	v_mfma_f32_16x16x32_bf16 v[70:73], v[170:173], v[210:213], v[70:73]
	v_mfma_f32_16x16x32_bf16 v[66:69], v[178:181], v[210:213], v[66:69]
	v_mfma_f32_16x16x32_bf16 v[118:121], v[174:177], v[190:193], v[118:121]
	v_mfma_f32_16x16x32_bf16 v[114:117], v[182:185], v[190:193], v[114:117]
	v_mfma_f32_16x16x32_bf16 v[102:105], v[174:177], v[198:201], v[102:105]
	v_mfma_f32_16x16x32_bf16 v[98:101], v[182:185], v[198:201], v[98:101]
	v_mfma_f32_16x16x32_bf16 v[86:89], v[174:177], v[206:209], v[86:89]
	v_mfma_f32_16x16x32_bf16 v[82:85], v[182:185], v[206:209], v[82:85]
	v_mfma_f32_16x16x32_bf16 v[70:73], v[174:177], v[214:217], v[70:73]
	v_mfma_f32_16x16x32_bf16 v[66:69], v[182:185], v[214:217], v[66:69]
	s_setprio 0
	s_barrier
	s_add_i32 s2, s51, s43
	v_lshl_add_u64 v[138:139], s[36:37], 0, v[142:143]
	s_mov_b32 m0, s2
	ds_read_b128 v[186:189], v161 offset:16384
	ds_read_b128 v[190:193], v161 offset:17408
	ds_read_b128 v[194:197], v161 offset:18432
	ds_read_b128 v[198:201], v161 offset:19456
	ds_read_b128 v[202:205], v161 offset:20480
	ds_read_b128 v[206:209], v161 offset:21504
	ds_read_b128 v[210:213], v161 offset:22528
	ds_read_b128 v[214:217], v161 offset:23552
	global_load_lds_dwordx4 v[138:139], off
	s_add_i32 m0, s2, 0x2000
	s_add_u32 s58, s36, 0x80000
	v_lshl_add_u64 v[154:155], s[36:37], 0, v[146:147]
	s_addc_u32 s59, s37, 0
	s_add_i32 s2, s52, s43
	global_load_lds_dwordx4 v[154:155], off
	v_lshl_add_u64 v[218:219], s[58:59], 0, v[142:143]
	s_mov_b32 m0, s2
	v_lshl_add_u64 v[220:221], s[38:39], 0, v[144:145]
	global_load_lds_dwordx4 v[218:219], off
	v_lshl_add_u64 v[218:219], s[58:59], 0, v[146:147]
	s_add_i32 m0, s2, 0x2000
	s_nop 0
	global_load_lds_dwordx4 v[218:219], off
	v_lshl_add_u64 v[218:219], s[38:39], 0, v[140:141]
	s_mov_b32 m0, s44
	s_nop 0
	global_load_lds_dwordx4 v[218:219], off
	s_mov_b32 m0, s45
	s_nop 0
	global_load_lds_dwordx4 v[220:221], off
	s_waitcnt vmcnt(8)
	s_waitcnt lgkmcnt(0)
	s_barrier
	s_setprio 1
	s_waitcnt lgkmcnt(0)
	v_mfma_f32_16x16x32_bf16 v[62:65], v[130:133], v[186:189], v[62:65]
	v_mfma_f32_16x16x32_bf16 v[58:61], v[162:165], v[186:189], v[58:61]
	v_mfma_f32_16x16x32_bf16 v[46:49], v[130:133], v[194:197], v[46:49]
	v_mfma_f32_16x16x32_bf16 v[42:45], v[162:165], v[194:197], v[42:45]
	v_mfma_f32_16x16x32_bf16 v[30:33], v[130:133], v[202:205], v[30:33]
	v_mfma_f32_16x16x32_bf16 v[26:29], v[162:165], v[202:205], v[26:29]
	v_mfma_f32_16x16x32_bf16 v[14:17], v[130:133], v[210:213], v[14:17]
	v_mfma_f32_16x16x32_bf16 v[10:13], v[162:165], v[210:213], v[10:13]
	v_mfma_f32_16x16x32_bf16 v[62:65], v[134:137], v[190:193], v[62:65]
	v_mfma_f32_16x16x32_bf16 v[58:61], v[166:169], v[190:193], v[58:61]
	v_mfma_f32_16x16x32_bf16 v[46:49], v[134:137], v[198:201], v[46:49]
	v_mfma_f32_16x16x32_bf16 v[42:45], v[166:169], v[198:201], v[42:45]
	v_mfma_f32_16x16x32_bf16 v[30:33], v[134:137], v[206:209], v[30:33]
	v_mfma_f32_16x16x32_bf16 v[26:29], v[166:169], v[206:209], v[26:29]
	v_mfma_f32_16x16x32_bf16 v[14:17], v[134:137], v[214:217], v[14:17]
	v_mfma_f32_16x16x32_bf16 v[10:13], v[166:169], v[214:217], v[10:13]
	s_setprio 0
	s_setprio 1
	v_mfma_f32_16x16x32_bf16 v[54:57], v[170:173], v[186:189], v[54:57]
	v_mfma_f32_16x16x32_bf16 v[50:53], v[178:181], v[186:189], v[50:53]
	v_mfma_f32_16x16x32_bf16 v[38:41], v[170:173], v[194:197], v[38:41]
	v_mfma_f32_16x16x32_bf16 v[34:37], v[178:181], v[194:197], v[34:37]
	v_mfma_f32_16x16x32_bf16 v[22:25], v[170:173], v[202:205], v[22:25]
	v_mfma_f32_16x16x32_bf16 v[18:21], v[178:181], v[202:205], v[18:21]
	v_mfma_f32_16x16x32_bf16 v[6:9], v[170:173], v[210:213], v[6:9]
	v_mfma_f32_16x16x32_bf16 v[2:5], v[178:181], v[210:213], v[2:5]
	v_mfma_f32_16x16x32_bf16 v[54:57], v[174:177], v[190:193], v[54:57]
	v_mfma_f32_16x16x32_bf16 v[50:53], v[182:185], v[190:193], v[50:53]
	v_mfma_f32_16x16x32_bf16 v[38:41], v[174:177], v[198:201], v[38:41]
	v_mfma_f32_16x16x32_bf16 v[34:37], v[182:185], v[198:201], v[34:37]
	v_mfma_f32_16x16x32_bf16 v[22:25], v[174:177], v[206:209], v[22:25]
	v_mfma_f32_16x16x32_bf16 v[18:21], v[182:185], v[206:209], v[18:21]
	v_mfma_f32_16x16x32_bf16 v[6:9], v[174:177], v[214:217], v[6:9]
	v_mfma_f32_16x16x32_bf16 v[2:5], v[182:185], v[214:217], v[2:5]
	s_setprio 0
	s_barrier
	s_add_i32 s2, 0, 0x18000
	v_add_u32_e32 v148, s2, v157
	s_add_i32 s3, 0, 0x1c000
	ds_read_b128 v[130:133], v148
	ds_read_b128 v[134:137], v148 offset:1024
	ds_read_b128 v[162:165], v148 offset:2048
	ds_read_b128 v[166:169], v148 offset:3072
	v_add_u32_e32 v148, s3, v157
	ds_read_b128 v[170:173], v148
	ds_read_b128 v[174:177], v148 offset:1024
	ds_read_b128 v[178:181], v148 offset:2048
	ds_read_b128 v[182:185], v148 offset:3072
	s_add_u32 s38, s38, 0x80000
	s_addc_u32 s39, s39, 0
	s_mov_b32 m0, s46
	v_lshl_add_u64 v[222:223], s[38:39], 0, v[140:141]
	ds_read_b128 v[186:189], v161 offset:32768
	ds_read_b128 v[190:193], v161 offset:33792
	ds_read_b128 v[194:197], v161 offset:34816
	ds_read_b128 v[198:201], v161 offset:35840
	ds_read_b128 v[202:205], v161 offset:36864
	ds_read_b128 v[206:209], v161 offset:37888
	ds_read_b128 v[210:213], v161 offset:38912
	ds_read_b128 v[214:217], v161 offset:39936
	global_load_lds_dwordx4 v[222:223], off
	v_lshl_add_u64 v[222:223], s[38:39], 0, v[144:145]
	s_mov_b32 m0, s47
	s_nop 0
	global_load_lds_dwordx4 v[222:223], off
	s_waitcnt vmcnt(8)
	s_waitcnt lgkmcnt(0)
	s_barrier
	s_setprio 1
	s_waitcnt lgkmcnt(0)
	v_mfma_f32_16x16x32_bf16 v[126:129], v[130:133], v[186:189], v[126:129]
	v_mfma_f32_16x16x32_bf16 v[122:125], v[162:165], v[186:189], v[122:125]
	v_mfma_f32_16x16x32_bf16 v[110:113], v[130:133], v[194:197], v[110:113]
	v_mfma_f32_16x16x32_bf16 v[106:109], v[162:165], v[194:197], v[106:109]
	v_mfma_f32_16x16x32_bf16 v[94:97], v[130:133], v[202:205], v[94:97]
	v_mfma_f32_16x16x32_bf16 v[90:93], v[162:165], v[202:205], v[90:93]
	v_mfma_f32_16x16x32_bf16 v[78:81], v[130:133], v[210:213], v[78:81]
	v_mfma_f32_16x16x32_bf16 v[74:77], v[162:165], v[210:213], v[74:77]
	v_mfma_f32_16x16x32_bf16 v[126:129], v[134:137], v[190:193], v[126:129]
	v_mfma_f32_16x16x32_bf16 v[122:125], v[166:169], v[190:193], v[122:125]
	v_mfma_f32_16x16x32_bf16 v[110:113], v[134:137], v[198:201], v[110:113]
	v_mfma_f32_16x16x32_bf16 v[106:109], v[166:169], v[198:201], v[106:109]
	v_mfma_f32_16x16x32_bf16 v[94:97], v[134:137], v[206:209], v[94:97]
	v_mfma_f32_16x16x32_bf16 v[90:93], v[166:169], v[206:209], v[90:93]
	v_mfma_f32_16x16x32_bf16 v[78:81], v[134:137], v[214:217], v[78:81]
	v_mfma_f32_16x16x32_bf16 v[74:77], v[166:169], v[214:217], v[74:77]
	s_setprio 0
	s_setprio 1
	v_mfma_f32_16x16x32_bf16 v[118:121], v[170:173], v[186:189], v[118:121]
	v_mfma_f32_16x16x32_bf16 v[114:117], v[178:181], v[186:189], v[114:117]
	v_mfma_f32_16x16x32_bf16 v[102:105], v[170:173], v[194:197], v[102:105]
	v_mfma_f32_16x16x32_bf16 v[98:101], v[178:181], v[194:197], v[98:101]
	v_mfma_f32_16x16x32_bf16 v[86:89], v[170:173], v[202:205], v[86:89]
	v_mfma_f32_16x16x32_bf16 v[82:85], v[178:181], v[202:205], v[82:85]
	v_mfma_f32_16x16x32_bf16 v[70:73], v[170:173], v[210:213], v[70:73]
	v_mfma_f32_16x16x32_bf16 v[66:69], v[178:181], v[210:213], v[66:69]
	v_mfma_f32_16x16x32_bf16 v[118:121], v[174:177], v[190:193], v[118:121]
	v_mfma_f32_16x16x32_bf16 v[114:117], v[182:185], v[190:193], v[114:117]
	v_mfma_f32_16x16x32_bf16 v[102:105], v[174:177], v[198:201], v[102:105]
	v_mfma_f32_16x16x32_bf16 v[98:101], v[182:185], v[198:201], v[98:101]
	v_mfma_f32_16x16x32_bf16 v[86:89], v[174:177], v[206:209], v[86:89]
	v_mfma_f32_16x16x32_bf16 v[82:85], v[182:185], v[206:209], v[82:85]
	v_mfma_f32_16x16x32_bf16 v[70:73], v[174:177], v[214:217], v[70:73]
	v_mfma_f32_16x16x32_bf16 v[66:69], v[182:185], v[214:217], v[66:69]
	s_setprio 0
	s_barrier
	s_add_i32 s2, s2, s43
	v_lshl_add_u64 v[138:139], v[138:139], 0, s[14:15]
	s_mov_b32 m0, s2
	ds_read_b128 v[186:189], v161 offset:49152
	ds_read_b128 v[190:193], v161 offset:50176
	ds_read_b128 v[194:197], v161 offset:51200
	ds_read_b128 v[198:201], v161 offset:52224
	ds_read_b128 v[202:205], v161 offset:53248
	ds_read_b128 v[206:209], v161 offset:54272
	ds_read_b128 v[210:213], v161 offset:55296
	ds_read_b128 v[214:217], v161 offset:56320
	global_load_lds_dwordx4 v[138:139], off
	s_add_i32 m0, s2, 0x2000
	s_add_u32 s36, s36, 0x80080
	v_lshl_add_u64 v[138:139], v[154:155], 0, s[14:15]
	s_addc_u32 s37, s37, 0
	s_add_i32 s2, s3, s43
	global_load_lds_dwordx4 v[138:139], off
	v_lshl_add_u64 v[138:139], s[36:37], 0, v[142:143]
	s_mov_b32 m0, s2
	s_nop 0
	global_load_lds_dwordx4 v[138:139], off
	v_lshl_add_u64 v[138:139], s[36:37], 0, v[146:147]
	s_add_i32 m0, s2, 0x2000
	s_nop 0
	global_load_lds_dwordx4 v[138:139], off
	v_lshl_add_u64 v[138:139], v[218:219], 0, s[14:15]
	s_mov_b32 m0, s49
	s_nop 0
	global_load_lds_dwordx4 v[138:139], off
	v_lshl_add_u64 v[138:139], v[220:221], 0, s[14:15]
	s_mov_b32 m0, s50
	s_nop 0
	global_load_lds_dwordx4 v[138:139], off
	s_waitcnt vmcnt(8)
	s_waitcnt lgkmcnt(0)
	s_barrier
	s_setprio 1
	s_waitcnt lgkmcnt(0)
	v_mfma_f32_16x16x32_bf16 v[62:65], v[130:133], v[186:189], v[62:65]
	v_mfma_f32_16x16x32_bf16 v[58:61], v[162:165], v[186:189], v[58:61]
	v_mfma_f32_16x16x32_bf16 v[46:49], v[130:133], v[194:197], v[46:49]
	v_mfma_f32_16x16x32_bf16 v[42:45], v[162:165], v[194:197], v[42:45]
	v_mfma_f32_16x16x32_bf16 v[30:33], v[130:133], v[202:205], v[30:33]
	v_mfma_f32_16x16x32_bf16 v[26:29], v[162:165], v[202:205], v[26:29]
	v_mfma_f32_16x16x32_bf16 v[14:17], v[130:133], v[210:213], v[14:17]
	v_mfma_f32_16x16x32_bf16 v[10:13], v[162:165], v[210:213], v[10:13]
	v_mfma_f32_16x16x32_bf16 v[62:65], v[134:137], v[190:193], v[62:65]
	v_mfma_f32_16x16x32_bf16 v[58:61], v[166:169], v[190:193], v[58:61]
	v_mfma_f32_16x16x32_bf16 v[46:49], v[134:137], v[198:201], v[46:49]
	v_mfma_f32_16x16x32_bf16 v[42:45], v[166:169], v[198:201], v[42:45]
	v_mfma_f32_16x16x32_bf16 v[30:33], v[134:137], v[206:209], v[30:33]
	v_mfma_f32_16x16x32_bf16 v[26:29], v[166:169], v[206:209], v[26:29]
	v_mfma_f32_16x16x32_bf16 v[14:17], v[134:137], v[214:217], v[14:17]
	v_mfma_f32_16x16x32_bf16 v[10:13], v[166:169], v[214:217], v[10:13]
	s_setprio 0
	s_setprio 1
	v_mfma_f32_16x16x32_bf16 v[54:57], v[170:173], v[186:189], v[54:57]
	v_mfma_f32_16x16x32_bf16 v[50:53], v[178:181], v[186:189], v[50:53]
	v_mfma_f32_16x16x32_bf16 v[38:41], v[170:173], v[194:197], v[38:41]
	v_mfma_f32_16x16x32_bf16 v[34:37], v[178:181], v[194:197], v[34:37]
	v_mfma_f32_16x16x32_bf16 v[22:25], v[170:173], v[202:205], v[22:25]
	v_mfma_f32_16x16x32_bf16 v[18:21], v[178:181], v[202:205], v[18:21]
	v_mfma_f32_16x16x32_bf16 v[6:9], v[170:173], v[210:213], v[6:9]
	v_mfma_f32_16x16x32_bf16 v[2:5], v[178:181], v[210:213], v[2:5]
	v_mfma_f32_16x16x32_bf16 v[54:57], v[174:177], v[190:193], v[54:57]
	v_mfma_f32_16x16x32_bf16 v[50:53], v[182:185], v[190:193], v[50:53]
	v_mfma_f32_16x16x32_bf16 v[38:41], v[174:177], v[198:201], v[38:41]
	v_mfma_f32_16x16x32_bf16 v[34:37], v[182:185], v[198:201], v[34:37]
	v_mfma_f32_16x16x32_bf16 v[22:25], v[174:177], v[206:209], v[22:25]
	v_mfma_f32_16x16x32_bf16 v[18:21], v[182:185], v[206:209], v[18:21]
	v_mfma_f32_16x16x32_bf16 v[6:9], v[174:177], v[214:217], v[6:9]
	v_mfma_f32_16x16x32_bf16 v[2:5], v[182:185], v[214:217], v[2:5]
	s_setprio 0
	s_add_i32 s56, s56, 2
	s_add_u32 s54, s54, 0x100
	s_addc_u32 s55, s55, 0
	s_add_u32 s34, s34, 0x100
	s_addc_u32 s35, s35, 0
	s_cmp_gt_u32 s56, 29
	s_barrier
	s_cbranch_scc0 .LBB0_227
	s_and_b64 vcc, exec, s[16:17]
	s_cbranch_vccz .LBB0_230
	s_barrier

.LBB0_1481:
	ds_read_b128 v[144:147], v162
	ds_read_b128 v[148:151], v162 offset:1024
	ds_read_b128 v[152:155], v162 offset:2048
	ds_read_b128 v[156:159], v162 offset:3072
	ds_read_b128 v[166:169], v163
	ds_read_b128 v[170:173], v163 offset:1024
	ds_read_b128 v[174:177], v163 offset:2048
	ds_read_b128 v[178:181], v163 offset:3072
	s_add_u32 s2, s26, 0xfff80080
	s_addc_u32 s3, s27, -1
	s_cmp_eq_u32 s50, 28
	s_cselect_b32 s31, s11, s3
	s_cselect_b32 s30, s17, s2
	s_cselect_b32 s29, s19, s49
	s_cselect_b32 s28, s25, s48
	v_lshl_add_u64 v[214:215], s[26:27], 0, v[142:143]
	s_add_i32 m0, s40, 0xc000
	ds_read_b128 v[182:185], v164
	ds_read_b128 v[186:189], v164 offset:1024
	ds_read_b128 v[190:193], v164 offset:2048
	ds_read_b128 v[194:197], v164 offset:3072
	ds_read_b128 v[198:201], v164 offset:4096
	ds_read_b128 v[202:205], v164 offset:5120
	ds_read_b128 v[206:209], v164 offset:6144
	ds_read_b128 v[210:213], v164 offset:7168
	global_load_lds_dwordx4 v[214:215], off
	v_lshl_add_u64 v[214:215], s[26:27], 0, v[140:141]
	s_add_i32 m0, s40, 0xe000
	s_nop 0
	global_load_lds_dwordx4 v[214:215], off
	s_waitcnt vmcnt(8)
	s_waitcnt lgkmcnt(0)
	s_barrier
	s_setprio 1
	s_waitcnt lgkmcnt(0)
	v_mfma_f32_16x16x32_bf16 v[126:129], v[144:147], v[182:185], v[126:129]
	v_mfma_f32_16x16x32_bf16 v[122:125], v[152:155], v[182:185], v[122:125]
	v_mfma_f32_16x16x32_bf16 v[110:113], v[144:147], v[190:193], v[110:113]
	v_mfma_f32_16x16x32_bf16 v[106:109], v[152:155], v[190:193], v[106:109]
	v_mfma_f32_16x16x32_bf16 v[94:97], v[144:147], v[198:201], v[94:97]
	v_mfma_f32_16x16x32_bf16 v[90:93], v[152:155], v[198:201], v[90:93]
	v_mfma_f32_16x16x32_bf16 v[78:81], v[144:147], v[206:209], v[78:81]
	v_mfma_f32_16x16x32_bf16 v[74:77], v[152:155], v[206:209], v[74:77]
	v_mfma_f32_16x16x32_bf16 v[126:129], v[148:151], v[186:189], v[126:129]
	v_mfma_f32_16x16x32_bf16 v[122:125], v[156:159], v[186:189], v[122:125]
	v_mfma_f32_16x16x32_bf16 v[110:113], v[148:151], v[194:197], v[110:113]
	v_mfma_f32_16x16x32_bf16 v[106:109], v[156:159], v[194:197], v[106:109]
	v_mfma_f32_16x16x32_bf16 v[94:97], v[148:151], v[202:205], v[94:97]
	v_mfma_f32_16x16x32_bf16 v[90:93], v[156:159], v[202:205], v[90:93]
	v_mfma_f32_16x16x32_bf16 v[78:81], v[148:151], v[210:213], v[78:81]
	v_mfma_f32_16x16x32_bf16 v[74:77], v[156:159], v[210:213], v[74:77]
	s_setprio 0
	s_setprio 1
	v_mfma_f32_16x16x32_bf16 v[118:121], v[166:169], v[182:185], v[118:121]
	v_mfma_f32_16x16x32_bf16 v[114:117], v[174:177], v[182:185], v[114:117]
	v_mfma_f32_16x16x32_bf16 v[102:105], v[166:169], v[190:193], v[102:105]
	v_mfma_f32_16x16x32_bf16 v[98:101], v[174:177], v[190:193], v[98:101]
	v_mfma_f32_16x16x32_bf16 v[86:89], v[166:169], v[198:201], v[86:89]
	v_mfma_f32_16x16x32_bf16 v[82:85], v[174:177], v[198:201], v[82:85]
	v_mfma_f32_16x16x32_bf16 v[70:73], v[166:169], v[206:209], v[70:73]
	v_mfma_f32_16x16x32_bf16 v[66:69], v[174:177], v[206:209], v[66:69]
	v_mfma_f32_16x16x32_bf16 v[118:121], v[170:173], v[186:189], v[118:121]
	v_mfma_f32_16x16x32_bf16 v[114:117], v[178:181], v[186:189], v[114:117]
	v_mfma_f32_16x16x32_bf16 v[102:105], v[170:173], v[194:197], v[102:105]
	v_mfma_f32_16x16x32_bf16 v[98:101], v[178:181], v[194:197], v[98:101]
	v_mfma_f32_16x16x32_bf16 v[86:89], v[170:173], v[202:205], v[86:89]
	v_mfma_f32_16x16x32_bf16 v[82:85], v[178:181], v[202:205], v[82:85]
	v_mfma_f32_16x16x32_bf16 v[70:73], v[170:173], v[210:213], v[70:73]
	v_mfma_f32_16x16x32_bf16 v[66:69], v[178:181], v[210:213], v[66:69]
	s_setprio 0
	s_barrier
	s_add_i32 s2, s46, s38
	v_lshl_add_u64 v[214:215], s[28:29], 0, v[132:133]
	s_mov_b32 m0, s2
	ds_read_b128 v[182:185], v164 offset:16384
	ds_read_b128 v[186:189], v164 offset:17408
	ds_read_b128 v[190:193], v164 offset:18432
	ds_read_b128 v[194:197], v164 offset:19456
	ds_read_b128 v[198:201], v164 offset:20480
	ds_read_b128 v[202:205], v164 offset:21504
	ds_read_b128 v[206:209], v164 offset:22528
	ds_read_b128 v[210:213], v164 offset:23552
	global_load_lds_dwordx4 v[214:215], off
	s_add_i32 m0, s2, 0x2000
	s_add_u32 s2, s28, 0x80000
	v_lshl_add_u64 v[216:217], s[28:29], 0, v[136:137]
	s_addc_u32 s3, s29, 0
	s_add_i32 s51, s47, s38
	global_load_lds_dwordx4 v[216:217], off
	v_lshl_add_u64 v[218:219], s[2:3], 0, v[132:133]
	s_mov_b32 m0, s51
	v_lshl_add_u64 v[220:221], s[30:31], 0, v[134:135]
	global_load_lds_dwordx4 v[218:219], off
	v_lshl_add_u64 v[218:219], s[2:3], 0, v[136:137]
	s_add_i32 m0, s51, 0x2000
	s_nop 0
	global_load_lds_dwordx4 v[218:219], off
	v_lshl_add_u64 v[218:219], s[30:31], 0, v[130:131]
	s_mov_b32 m0, s40
	s_nop 0
	global_load_lds_dwordx4 v[218:219], off
	s_mov_b32 m0, s41
	s_nop 0
	global_load_lds_dwordx4 v[220:221], off
	s_waitcnt vmcnt(8)
	s_waitcnt lgkmcnt(0)
	s_barrier
	s_setprio 1
	s_waitcnt lgkmcnt(0)
	v_mfma_f32_16x16x32_bf16 v[62:65], v[144:147], v[182:185], v[62:65]
	v_mfma_f32_16x16x32_bf16 v[58:61], v[152:155], v[182:185], v[58:61]
	v_mfma_f32_16x16x32_bf16 v[46:49], v[144:147], v[190:193], v[46:49]
	v_mfma_f32_16x16x32_bf16 v[42:45], v[152:155], v[190:193], v[42:45]
	v_mfma_f32_16x16x32_bf16 v[30:33], v[144:147], v[198:201], v[30:33]
	v_mfma_f32_16x16x32_bf16 v[26:29], v[152:155], v[198:201], v[26:29]
	v_mfma_f32_16x16x32_bf16 v[14:17], v[144:147], v[206:209], v[14:17]
	v_mfma_f32_16x16x32_bf16 v[10:13], v[152:155], v[206:209], v[10:13]
	v_mfma_f32_16x16x32_bf16 v[62:65], v[148:151], v[186:189], v[62:65]
	v_mfma_f32_16x16x32_bf16 v[58:61], v[156:159], v[186:189], v[58:61]
	v_mfma_f32_16x16x32_bf16 v[46:49], v[148:151], v[194:197], v[46:49]
	v_mfma_f32_16x16x32_bf16 v[42:45], v[156:159], v[194:197], v[42:45]
	v_mfma_f32_16x16x32_bf16 v[30:33], v[148:151], v[202:205], v[30:33]
	v_mfma_f32_16x16x32_bf16 v[26:29], v[156:159], v[202:205], v[26:29]
	v_mfma_f32_16x16x32_bf16 v[14:17], v[148:151], v[210:213], v[14:17]
	v_mfma_f32_16x16x32_bf16 v[10:13], v[156:159], v[210:213], v[10:13]
	s_setprio 0
	s_setprio 1
	v_mfma_f32_16x16x32_bf16 v[54:57], v[166:169], v[182:185], v[54:57]
	v_mfma_f32_16x16x32_bf16 v[50:53], v[174:177], v[182:185], v[50:53]
	v_mfma_f32_16x16x32_bf16 v[38:41], v[166:169], v[190:193], v[38:41]
	v_mfma_f32_16x16x32_bf16 v[34:37], v[174:177], v[190:193], v[34:37]
	v_mfma_f32_16x16x32_bf16 v[22:25], v[166:169], v[198:201], v[22:25]
	v_mfma_f32_16x16x32_bf16 v[18:21], v[174:177], v[198:201], v[18:21]
	v_mfma_f32_16x16x32_bf16 v[6:9], v[166:169], v[206:209], v[6:9]
	v_mfma_f32_16x16x32_bf16 v[2:5], v[174:177], v[206:209], v[2:5]
	v_mfma_f32_16x16x32_bf16 v[54:57], v[170:173], v[186:189], v[54:57]
	v_mfma_f32_16x16x32_bf16 v[50:53], v[178:181], v[186:189], v[50:53]
	v_mfma_f32_16x16x32_bf16 v[38:41], v[170:173], v[194:197], v[38:41]
	v_mfma_f32_16x16x32_bf16 v[34:37], v[178:181], v[194:197], v[34:37]
	v_mfma_f32_16x16x32_bf16 v[22:25], v[170:173], v[202:205], v[22:25]
	v_mfma_f32_16x16x32_bf16 v[18:21], v[178:181], v[202:205], v[18:21]
	v_mfma_f32_16x16x32_bf16 v[6:9], v[170:173], v[210:213], v[6:9]
	v_mfma_f32_16x16x32_bf16 v[2:5], v[178:181], v[210:213], v[2:5]
	s_setprio 0
	s_barrier
	s_add_i32 s51, 0, 0x18000
	s_add_i32 s52, 0, 0x1c000
	v_add_u32_e32 v156, s51, v160
	v_add_u32_e32 v165, s52, v160
	ds_read_b128 v[144:147], v156
	ds_read_b128 v[148:151], v156 offset:1024
	ds_read_b128 v[152:155], v156 offset:2048
	ds_read_b128 v[156:159], v156 offset:3072
	ds_read_b128 v[166:169], v165
	ds_read_b128 v[170:173], v165 offset:1024
	ds_read_b128 v[174:177], v165 offset:2048
	ds_read_b128 v[178:181], v165 offset:3072
	s_add_u32 s2, s30, 0x80000
	s_addc_u32 s3, s31, 0
	s_mov_b32 m0, s42
	v_lshl_add_u64 v[222:223], s[2:3], 0, v[130:131]
	ds_read_b128 v[182:185], v164 offset:32768
	ds_read_b128 v[186:189], v164 offset:33792
	ds_read_b128 v[190:193], v164 offset:34816
	ds_read_b128 v[194:197], v164 offset:35840
	ds_read_b128 v[198:201], v164 offset:36864
	ds_read_b128 v[202:205], v164 offset:37888
	ds_read_b128 v[206:209], v164 offset:38912
	ds_read_b128 v[210:213], v164 offset:39936
	global_load_lds_dwordx4 v[222:223], off
	v_lshl_add_u64 v[222:223], s[2:3], 0, v[134:135]
	s_mov_b32 m0, s43
	s_nop 0
	global_load_lds_dwordx4 v[222:223], off
	s_waitcnt vmcnt(8)
	s_waitcnt lgkmcnt(0)
	s_barrier
	s_setprio 1
	s_waitcnt lgkmcnt(0)
	v_mfma_f32_16x16x32_bf16 v[126:129], v[144:147], v[182:185], v[126:129]
	v_mfma_f32_16x16x32_bf16 v[122:125], v[152:155], v[182:185], v[122:125]
	v_mfma_f32_16x16x32_bf16 v[110:113], v[144:147], v[190:193], v[110:113]
	v_mfma_f32_16x16x32_bf16 v[106:109], v[152:155], v[190:193], v[106:109]
	v_mfma_f32_16x16x32_bf16 v[94:97], v[144:147], v[198:201], v[94:97]
	v_mfma_f32_16x16x32_bf16 v[90:93], v[152:155], v[198:201], v[90:93]
	v_mfma_f32_16x16x32_bf16 v[78:81], v[144:147], v[206:209], v[78:81]
	v_mfma_f32_16x16x32_bf16 v[74:77], v[152:155], v[206:209], v[74:77]
	v_mfma_f32_16x16x32_bf16 v[126:129], v[148:151], v[186:189], v[126:129]
	v_mfma_f32_16x16x32_bf16 v[122:125], v[156:159], v[186:189], v[122:125]
	v_mfma_f32_16x16x32_bf16 v[110:113], v[148:151], v[194:197], v[110:113]
	v_mfma_f32_16x16x32_bf16 v[106:109], v[156:159], v[194:197], v[106:109]
	v_mfma_f32_16x16x32_bf16 v[94:97], v[148:151], v[202:205], v[94:97]
	v_mfma_f32_16x16x32_bf16 v[90:93], v[156:159], v[202:205], v[90:93]
	v_mfma_f32_16x16x32_bf16 v[78:81], v[148:151], v[210:213], v[78:81]
	v_mfma_f32_16x16x32_bf16 v[74:77], v[156:159], v[210:213], v[74:77]
	s_setprio 0
	s_setprio 1
	v_mfma_f32_16x16x32_bf16 v[118:121], v[166:169], v[182:185], v[118:121]
	v_mfma_f32_16x16x32_bf16 v[114:117], v[174:177], v[182:185], v[114:117]
	v_mfma_f32_16x16x32_bf16 v[102:105], v[166:169], v[190:193], v[102:105]
	v_mfma_f32_16x16x32_bf16 v[98:101], v[174:177], v[190:193], v[98:101]
	v_mfma_f32_16x16x32_bf16 v[86:89], v[166:169], v[198:201], v[86:89]
	v_mfma_f32_16x16x32_bf16 v[82:85], v[174:177], v[198:201], v[82:85]
	v_mfma_f32_16x16x32_bf16 v[70:73], v[166:169], v[206:209], v[70:73]
	v_mfma_f32_16x16x32_bf16 v[66:69], v[174:177], v[206:209], v[66:69]
	v_mfma_f32_16x16x32_bf16 v[118:121], v[170:173], v[186:189], v[118:121]
	v_mfma_f32_16x16x32_bf16 v[114:117], v[178:181], v[186:189], v[114:117]
	v_mfma_f32_16x16x32_bf16 v[102:105], v[170:173], v[194:197], v[102:105]
	v_mfma_f32_16x16x32_bf16 v[98:101], v[178:181], v[194:197], v[98:101]
	v_mfma_f32_16x16x32_bf16 v[86:89], v[170:173], v[202:205], v[86:89]
	v_mfma_f32_16x16x32_bf16 v[82:85], v[178:181], v[202:205], v[82:85]
	v_mfma_f32_16x16x32_bf16 v[70:73], v[170:173], v[210:213], v[70:73]
	v_mfma_f32_16x16x32_bf16 v[66:69], v[178:181], v[210:213], v[66:69]
	s_setprio 0
	s_barrier
	s_add_i32 s2, s51, s38
	v_lshl_add_u64 v[214:215], v[214:215], 0, s[6:7]
	s_mov_b32 m0, s2
	ds_read_b128 v[182:185], v164 offset:49152
	ds_read_b128 v[186:189], v164 offset:50176
	ds_read_b128 v[190:193], v164 offset:51200
	ds_read_b128 v[194:197], v164 offset:52224
	ds_read_b128 v[198:201], v164 offset:53248
	ds_read_b128 v[202:205], v164 offset:54272
	ds_read_b128 v[206:209], v164 offset:55296
	ds_read_b128 v[210:213], v164 offset:56320
	global_load_lds_dwordx4 v[214:215], off
	s_add_i32 m0, s2, 0x2000
	s_add_u32 s2, s28, 0x80080
	v_lshl_add_u64 v[214:215], v[216:217], 0, s[6:7]
	s_addc_u32 s3, s29, 0
	s_add_i32 s28, s52, s38
	global_load_lds_dwordx4 v[214:215], off
	v_lshl_add_u64 v[214:215], s[2:3], 0, v[132:133]
	s_mov_b32 m0, s28
	s_nop 0
	global_load_lds_dwordx4 v[214:215], off
	v_lshl_add_u64 v[214:215], s[2:3], 0, v[136:137]
	s_add_i32 m0, s28, 0x2000
	s_nop 0
	global_load_lds_dwordx4 v[214:215], off
	v_lshl_add_u64 v[214:215], v[218:219], 0, s[6:7]
	s_mov_b32 m0, s44
	s_nop 0
	global_load_lds_dwordx4 v[214:215], off
	v_lshl_add_u64 v[214:215], v[220:221], 0, s[6:7]
	s_mov_b32 m0, s45
	s_nop 0
	global_load_lds_dwordx4 v[214:215], off
	s_waitcnt vmcnt(8)
	s_waitcnt lgkmcnt(0)
	s_barrier
	s_setprio 1
	s_waitcnt lgkmcnt(0)
	v_mfma_f32_16x16x32_bf16 v[62:65], v[144:147], v[182:185], v[62:65]
	v_mfma_f32_16x16x32_bf16 v[58:61], v[152:155], v[182:185], v[58:61]
	v_mfma_f32_16x16x32_bf16 v[46:49], v[144:147], v[190:193], v[46:49]
	v_mfma_f32_16x16x32_bf16 v[42:45], v[152:155], v[190:193], v[42:45]
	v_mfma_f32_16x16x32_bf16 v[30:33], v[144:147], v[198:201], v[30:33]
	v_mfma_f32_16x16x32_bf16 v[26:29], v[152:155], v[198:201], v[26:29]
	v_mfma_f32_16x16x32_bf16 v[14:17], v[144:147], v[206:209], v[14:17]
	v_mfma_f32_16x16x32_bf16 v[10:13], v[152:155], v[206:209], v[10:13]
	v_mfma_f32_16x16x32_bf16 v[62:65], v[148:151], v[186:189], v[62:65]
	v_mfma_f32_16x16x32_bf16 v[58:61], v[156:159], v[186:189], v[58:61]
	v_mfma_f32_16x16x32_bf16 v[46:49], v[148:151], v[194:197], v[46:49]
	v_mfma_f32_16x16x32_bf16 v[42:45], v[156:159], v[194:197], v[42:45]
	v_mfma_f32_16x16x32_bf16 v[30:33], v[148:151], v[202:205], v[30:33]
	v_mfma_f32_16x16x32_bf16 v[26:29], v[156:159], v[202:205], v[26:29]
	v_mfma_f32_16x16x32_bf16 v[14:17], v[148:151], v[210:213], v[14:17]
	v_mfma_f32_16x16x32_bf16 v[10:13], v[156:159], v[210:213], v[10:13]
	s_setprio 0
	s_setprio 1
	v_mfma_f32_16x16x32_bf16 v[54:57], v[166:169], v[182:185], v[54:57]
	v_mfma_f32_16x16x32_bf16 v[50:53], v[174:177], v[182:185], v[50:53]
	v_mfma_f32_16x16x32_bf16 v[38:41], v[166:169], v[190:193], v[38:41]
	v_mfma_f32_16x16x32_bf16 v[34:37], v[174:177], v[190:193], v[34:37]
	v_mfma_f32_16x16x32_bf16 v[22:25], v[166:169], v[198:201], v[22:25]
	v_mfma_f32_16x16x32_bf16 v[18:21], v[174:177], v[198:201], v[18:21]
	v_mfma_f32_16x16x32_bf16 v[6:9], v[166:169], v[206:209], v[6:9]
	v_mfma_f32_16x16x32_bf16 v[2:5], v[174:177], v[206:209], v[2:5]
	v_mfma_f32_16x16x32_bf16 v[54:57], v[170:173], v[186:189], v[54:57]
	v_mfma_f32_16x16x32_bf16 v[50:53], v[178:181], v[186:189], v[50:53]
	v_mfma_f32_16x16x32_bf16 v[38:41], v[170:173], v[194:197], v[38:41]
	v_mfma_f32_16x16x32_bf16 v[34:37], v[178:181], v[194:197], v[34:37]
	v_mfma_f32_16x16x32_bf16 v[22:25], v[170:173], v[202:205], v[22:25]
	v_mfma_f32_16x16x32_bf16 v[18:21], v[178:181], v[202:205], v[18:21]
	v_mfma_f32_16x16x32_bf16 v[6:9], v[170:173], v[210:213], v[6:9]
	v_mfma_f32_16x16x32_bf16 v[2:5], v[178:181], v[210:213], v[2:5]
	s_setprio 0
	s_add_i32 s50, s50, 2
	s_add_u32 s48, s48, 0x100
	s_addc_u32 s49, s49, 0
	s_add_u32 s26, s26, 0x100
	s_addc_u32 s27, s27, 0
	s_cmp_gt_u32 s50, 29
	s_barrier
	s_cbranch_scc0 .LBB0_1481
	s_and_b64 vcc, exec, s[12:13]
	s_cbranch_vccz .LBB0_1484
	s_barrier

.LBB0_2088:
	ds_read_b128 v[150:153], v147
	ds_read_b128 v[154:157], v147 offset:1024
	ds_read_b128 v[158:161], v147 offset:2048
	ds_read_b128 v[162:165], v147 offset:3072
	ds_read_b128 v[166:169], v148
	ds_read_b128 v[170:173], v148 offset:1024
	ds_read_b128 v[174:177], v148 offset:2048
	ds_read_b128 v[178:181], v148 offset:3072
	s_add_u32 s2, s40, 0xfff80080
	s_addc_u32 s3, s41, -1
	s_cmp_eq_u32 s37, 28
	s_cselect_b32 s45, s6, s3
	s_cselect_b32 s44, s25, s2
	s_cselect_b32 s43, s31, s29
	s_cselect_b32 s42, s30, s27
	v_lshl_add_u64 v[142:143], s[40:41], 0, v[140:141]
	s_add_i32 m0, s39, 0xc000
	ds_read_b128 v[182:185], v149
	ds_read_b128 v[186:189], v149 offset:1024
	ds_read_b128 v[190:193], v149 offset:2048
	ds_read_b128 v[194:197], v149 offset:3072
	ds_read_b128 v[198:201], v149 offset:4096
	ds_read_b128 v[202:205], v149 offset:5120
	ds_read_b128 v[206:209], v149 offset:6144
	ds_read_b128 v[210:213], v149 offset:7168
	global_load_lds_dwordx4 v[142:143], off
	v_lshl_add_u64 v[142:143], s[40:41], 0, v[138:139]
	s_add_i32 m0, s39, 0xe000
	s_nop 0
	global_load_lds_dwordx4 v[142:143], off
	s_waitcnt vmcnt(8)
	s_waitcnt lgkmcnt(0)
	s_barrier
	s_setprio 1
	s_waitcnt lgkmcnt(0)
	v_mfma_f32_16x16x32_bf16 v[126:129], v[150:153], v[182:185], v[126:129]
	v_mfma_f32_16x16x32_bf16 v[118:121], v[158:161], v[182:185], v[118:121]
	v_mfma_f32_16x16x32_bf16 v[110:113], v[150:153], v[190:193], v[110:113]
	v_mfma_f32_16x16x32_bf16 v[102:105], v[158:161], v[190:193], v[102:105]
	v_mfma_f32_16x16x32_bf16 v[94:97], v[150:153], v[198:201], v[94:97]
	v_mfma_f32_16x16x32_bf16 v[86:89], v[158:161], v[198:201], v[86:89]
	v_mfma_f32_16x16x32_bf16 v[78:81], v[150:153], v[206:209], v[78:81]
	v_mfma_f32_16x16x32_bf16 v[70:73], v[158:161], v[206:209], v[70:73]
	v_mfma_f32_16x16x32_bf16 v[126:129], v[154:157], v[186:189], v[126:129]
	v_mfma_f32_16x16x32_bf16 v[118:121], v[162:165], v[186:189], v[118:121]
	v_mfma_f32_16x16x32_bf16 v[110:113], v[154:157], v[194:197], v[110:113]
	v_mfma_f32_16x16x32_bf16 v[102:105], v[162:165], v[194:197], v[102:105]
	v_mfma_f32_16x16x32_bf16 v[94:97], v[154:157], v[202:205], v[94:97]
	v_mfma_f32_16x16x32_bf16 v[86:89], v[162:165], v[202:205], v[86:89]
	v_mfma_f32_16x16x32_bf16 v[78:81], v[154:157], v[210:213], v[78:81]
	v_mfma_f32_16x16x32_bf16 v[70:73], v[162:165], v[210:213], v[70:73]
	s_setprio 0
	s_setprio 1
	v_mfma_f32_16x16x32_bf16 v[122:125], v[166:169], v[182:185], v[122:125]
	v_mfma_f32_16x16x32_bf16 v[114:117], v[174:177], v[182:185], v[114:117]
	v_mfma_f32_16x16x32_bf16 v[106:109], v[166:169], v[190:193], v[106:109]
	v_mfma_f32_16x16x32_bf16 v[98:101], v[174:177], v[190:193], v[98:101]
	v_mfma_f32_16x16x32_bf16 v[90:93], v[166:169], v[198:201], v[90:93]
	v_mfma_f32_16x16x32_bf16 v[82:85], v[174:177], v[198:201], v[82:85]
	v_mfma_f32_16x16x32_bf16 v[74:77], v[166:169], v[206:209], v[74:77]
	v_mfma_f32_16x16x32_bf16 v[66:69], v[174:177], v[206:209], v[66:69]
	v_mfma_f32_16x16x32_bf16 v[122:125], v[170:173], v[186:189], v[122:125]
	v_mfma_f32_16x16x32_bf16 v[114:117], v[178:181], v[186:189], v[114:117]
	v_mfma_f32_16x16x32_bf16 v[106:109], v[170:173], v[194:197], v[106:109]
	v_mfma_f32_16x16x32_bf16 v[98:101], v[178:181], v[194:197], v[98:101]
	v_mfma_f32_16x16x32_bf16 v[90:93], v[170:173], v[202:205], v[90:93]
	v_mfma_f32_16x16x32_bf16 v[82:85], v[178:181], v[202:205], v[82:85]
	v_mfma_f32_16x16x32_bf16 v[74:77], v[170:173], v[210:213], v[74:77]
	v_mfma_f32_16x16x32_bf16 v[66:69], v[178:181], v[210:213], v[66:69]
	s_setprio 0
	s_barrier
	s_add_i32 s2, s57, s48
	v_lshl_add_u64 v[142:143], s[42:43], 0, v[132:133]
	s_mov_b32 m0, s2
	ds_read_b128 v[182:185], v149 offset:16384
	ds_read_b128 v[186:189], v149 offset:17408
	ds_read_b128 v[190:193], v149 offset:18432
	ds_read_b128 v[194:197], v149 offset:19456
	ds_read_b128 v[198:201], v149 offset:20480
	ds_read_b128 v[202:205], v149 offset:21504
	ds_read_b128 v[206:209], v149 offset:22528
	ds_read_b128 v[210:213], v149 offset:23552
	global_load_lds_dwordx4 v[142:143], off
	s_add_i32 m0, s2, 0x2000
	s_add_u32 s2, s42, 0x80000
	v_lshl_add_u64 v[214:215], s[42:43], 0, v[136:137]
	s_addc_u32 s3, s43, 0
	s_add_i32 s46, s58, s48
	global_load_lds_dwordx4 v[214:215], off
	v_lshl_add_u64 v[216:217], s[2:3], 0, v[132:133]
	s_mov_b32 m0, s46
	v_lshl_add_u64 v[218:219], s[44:45], 0, v[134:135]
	global_load_lds_dwordx4 v[216:217], off
	v_lshl_add_u64 v[216:217], s[2:3], 0, v[136:137]
	s_add_i32 m0, s46, 0x2000
	s_nop 0
	global_load_lds_dwordx4 v[216:217], off
	v_lshl_add_u64 v[216:217], s[44:45], 0, v[130:131]
	s_mov_b32 m0, s39
	s_nop 0
	global_load_lds_dwordx4 v[216:217], off
	s_mov_b32 m0, s49
	s_nop 0
	global_load_lds_dwordx4 v[218:219], off
	s_waitcnt vmcnt(8)
	s_waitcnt lgkmcnt(0)
	s_barrier
	s_setprio 1
	s_waitcnt lgkmcnt(0)
	v_mfma_f32_16x16x32_bf16 v[62:65], v[150:153], v[182:185], v[62:65]
	v_mfma_f32_16x16x32_bf16 v[54:57], v[158:161], v[182:185], v[54:57]
	v_mfma_f32_16x16x32_bf16 v[46:49], v[150:153], v[190:193], v[46:49]
	v_mfma_f32_16x16x32_bf16 v[38:41], v[158:161], v[190:193], v[38:41]
	v_mfma_f32_16x16x32_bf16 v[30:33], v[150:153], v[198:201], v[30:33]
	v_mfma_f32_16x16x32_bf16 v[22:25], v[158:161], v[198:201], v[22:25]
	v_mfma_f32_16x16x32_bf16 v[14:17], v[150:153], v[206:209], v[14:17]
	v_mfma_f32_16x16x32_bf16 v[6:9], v[158:161], v[206:209], v[6:9]
	v_mfma_f32_16x16x32_bf16 v[62:65], v[154:157], v[186:189], v[62:65]
	v_mfma_f32_16x16x32_bf16 v[54:57], v[162:165], v[186:189], v[54:57]
	v_mfma_f32_16x16x32_bf16 v[46:49], v[154:157], v[194:197], v[46:49]
	v_mfma_f32_16x16x32_bf16 v[38:41], v[162:165], v[194:197], v[38:41]
	v_mfma_f32_16x16x32_bf16 v[30:33], v[154:157], v[202:205], v[30:33]
	v_mfma_f32_16x16x32_bf16 v[22:25], v[162:165], v[202:205], v[22:25]
	v_mfma_f32_16x16x32_bf16 v[14:17], v[154:157], v[210:213], v[14:17]
	v_mfma_f32_16x16x32_bf16 v[6:9], v[162:165], v[210:213], v[6:9]
	s_setprio 0
	s_setprio 1
	v_mfma_f32_16x16x32_bf16 v[58:61], v[166:169], v[182:185], v[58:61]
	v_mfma_f32_16x16x32_bf16 v[50:53], v[174:177], v[182:185], v[50:53]
	v_mfma_f32_16x16x32_bf16 v[42:45], v[166:169], v[190:193], v[42:45]
	v_mfma_f32_16x16x32_bf16 v[34:37], v[174:177], v[190:193], v[34:37]
	v_mfma_f32_16x16x32_bf16 v[26:29], v[166:169], v[198:201], v[26:29]
	v_mfma_f32_16x16x32_bf16 v[18:21], v[174:177], v[198:201], v[18:21]
	v_mfma_f32_16x16x32_bf16 v[10:13], v[166:169], v[206:209], v[10:13]
	v_mfma_f32_16x16x32_bf16 v[2:5], v[174:177], v[206:209], v[2:5]
	v_mfma_f32_16x16x32_bf16 v[58:61], v[170:173], v[186:189], v[58:61]
	v_mfma_f32_16x16x32_bf16 v[50:53], v[178:181], v[186:189], v[50:53]
	v_mfma_f32_16x16x32_bf16 v[42:45], v[170:173], v[194:197], v[42:45]
	v_mfma_f32_16x16x32_bf16 v[34:37], v[178:181], v[194:197], v[34:37]
	v_mfma_f32_16x16x32_bf16 v[26:29], v[170:173], v[202:205], v[26:29]
	v_mfma_f32_16x16x32_bf16 v[18:21], v[178:181], v[202:205], v[18:21]
	v_mfma_f32_16x16x32_bf16 v[10:13], v[170:173], v[210:213], v[10:13]
	v_mfma_f32_16x16x32_bf16 v[2:5], v[178:181], v[210:213], v[2:5]
	s_setprio 0
	s_barrier
	s_add_i32 s46, 0, 0x18000
	s_add_i32 s47, 0, 0x1c000
	v_add_u32_e32 v162, s46, v145
	v_add_u32_e32 v178, s47, v145
	ds_read_b128 v[150:153], v162
	ds_read_b128 v[154:157], v162 offset:1024
	ds_read_b128 v[158:161], v162 offset:2048
	ds_read_b128 v[162:165], v162 offset:3072
	ds_read_b128 v[166:169], v178
	ds_read_b128 v[170:173], v178 offset:1024
	ds_read_b128 v[174:177], v178 offset:2048
	ds_read_b128 v[178:181], v178 offset:3072
	s_add_u32 s2, s44, 0x80000
	s_addc_u32 s3, s45, 0
	s_mov_b32 m0, s50
	v_lshl_add_u64 v[220:221], s[2:3], 0, v[130:131]
	ds_read_b128 v[182:185], v149 offset:32768
	ds_read_b128 v[186:189], v149 offset:33792
	ds_read_b128 v[190:193], v149 offset:34816
	ds_read_b128 v[194:197], v149 offset:35840
	ds_read_b128 v[198:201], v149 offset:36864
	ds_read_b128 v[202:205], v149 offset:37888
	ds_read_b128 v[206:209], v149 offset:38912
	ds_read_b128 v[210:213], v149 offset:39936
	global_load_lds_dwordx4 v[220:221], off
	v_lshl_add_u64 v[220:221], s[2:3], 0, v[134:135]
	s_mov_b32 m0, s51
	s_nop 0
	global_load_lds_dwordx4 v[220:221], off
	s_waitcnt vmcnt(8)
	s_waitcnt lgkmcnt(0)
	s_barrier
	s_setprio 1
	s_waitcnt lgkmcnt(0)
	v_mfma_f32_16x16x32_bf16 v[126:129], v[150:153], v[182:185], v[126:129]
	v_mfma_f32_16x16x32_bf16 v[118:121], v[158:161], v[182:185], v[118:121]
	v_mfma_f32_16x16x32_bf16 v[110:113], v[150:153], v[190:193], v[110:113]
	v_mfma_f32_16x16x32_bf16 v[102:105], v[158:161], v[190:193], v[102:105]
	v_mfma_f32_16x16x32_bf16 v[94:97], v[150:153], v[198:201], v[94:97]
	v_mfma_f32_16x16x32_bf16 v[86:89], v[158:161], v[198:201], v[86:89]
	v_mfma_f32_16x16x32_bf16 v[78:81], v[150:153], v[206:209], v[78:81]
	v_mfma_f32_16x16x32_bf16 v[70:73], v[158:161], v[206:209], v[70:73]
	v_mfma_f32_16x16x32_bf16 v[126:129], v[154:157], v[186:189], v[126:129]
	v_mfma_f32_16x16x32_bf16 v[118:121], v[162:165], v[186:189], v[118:121]
	v_mfma_f32_16x16x32_bf16 v[110:113], v[154:157], v[194:197], v[110:113]
	v_mfma_f32_16x16x32_bf16 v[102:105], v[162:165], v[194:197], v[102:105]
	v_mfma_f32_16x16x32_bf16 v[94:97], v[154:157], v[202:205], v[94:97]
	v_mfma_f32_16x16x32_bf16 v[86:89], v[162:165], v[202:205], v[86:89]
	v_mfma_f32_16x16x32_bf16 v[78:81], v[154:157], v[210:213], v[78:81]
	v_mfma_f32_16x16x32_bf16 v[70:73], v[162:165], v[210:213], v[70:73]
	s_setprio 0
	s_setprio 1
	v_mfma_f32_16x16x32_bf16 v[122:125], v[166:169], v[182:185], v[122:125]
	v_mfma_f32_16x16x32_bf16 v[114:117], v[174:177], v[182:185], v[114:117]
	v_mfma_f32_16x16x32_bf16 v[106:109], v[166:169], v[190:193], v[106:109]
	v_mfma_f32_16x16x32_bf16 v[98:101], v[174:177], v[190:193], v[98:101]
	v_mfma_f32_16x16x32_bf16 v[90:93], v[166:169], v[198:201], v[90:93]
	v_mfma_f32_16x16x32_bf16 v[82:85], v[174:177], v[198:201], v[82:85]
	v_mfma_f32_16x16x32_bf16 v[74:77], v[166:169], v[206:209], v[74:77]
	v_mfma_f32_16x16x32_bf16 v[66:69], v[174:177], v[206:209], v[66:69]
	v_mfma_f32_16x16x32_bf16 v[122:125], v[170:173], v[186:189], v[122:125]
	v_mfma_f32_16x16x32_bf16 v[114:117], v[178:181], v[186:189], v[114:117]
	v_mfma_f32_16x16x32_bf16 v[106:109], v[170:173], v[194:197], v[106:109]
	v_mfma_f32_16x16x32_bf16 v[98:101], v[178:181], v[194:197], v[98:101]
	v_mfma_f32_16x16x32_bf16 v[90:93], v[170:173], v[202:205], v[90:93]
	v_mfma_f32_16x16x32_bf16 v[82:85], v[178:181], v[202:205], v[82:85]
	v_mfma_f32_16x16x32_bf16 v[74:77], v[170:173], v[210:213], v[74:77]
	v_mfma_f32_16x16x32_bf16 v[66:69], v[178:181], v[210:213], v[66:69]
	s_setprio 0
	s_barrier
	s_add_i32 s2, s46, s48
	v_lshl_add_u64 v[142:143], v[142:143], 0, s[20:21]
	s_mov_b32 m0, s2
	ds_read_b128 v[182:185], v149 offset:49152
	ds_read_b128 v[186:189], v149 offset:50176
	ds_read_b128 v[190:193], v149 offset:51200
	ds_read_b128 v[194:197], v149 offset:52224
	ds_read_b128 v[198:201], v149 offset:53248
	ds_read_b128 v[202:205], v149 offset:54272
	ds_read_b128 v[206:209], v149 offset:55296
	ds_read_b128 v[210:213], v149 offset:56320
	global_load_lds_dwordx4 v[142:143], off
	s_add_i32 m0, s2, 0x2000
	s_add_u32 s2, s42, 0x80080
	v_lshl_add_u64 v[142:143], v[214:215], 0, s[20:21]
	s_addc_u32 s3, s43, 0
	s_add_i32 s42, s47, s48
	global_load_lds_dwordx4 v[142:143], off
	v_lshl_add_u64 v[142:143], s[2:3], 0, v[132:133]
	s_mov_b32 m0, s42
	s_nop 0
	global_load_lds_dwordx4 v[142:143], off
	v_lshl_add_u64 v[142:143], s[2:3], 0, v[136:137]
	s_add_i32 m0, s42, 0x2000
	s_nop 0
	global_load_lds_dwordx4 v[142:143], off
	v_lshl_add_u64 v[142:143], v[216:217], 0, s[20:21]
	s_mov_b32 m0, s52
	s_nop 0
	global_load_lds_dwordx4 v[142:143], off
	v_lshl_add_u64 v[142:143], v[218:219], 0, s[20:21]
	s_mov_b32 m0, s53
	s_nop 0
	global_load_lds_dwordx4 v[142:143], off
	s_waitcnt vmcnt(8)
	s_waitcnt lgkmcnt(0)
	s_barrier
	s_setprio 1
	s_waitcnt lgkmcnt(0)
	v_mfma_f32_16x16x32_bf16 v[62:65], v[150:153], v[182:185], v[62:65]
	v_mfma_f32_16x16x32_bf16 v[54:57], v[158:161], v[182:185], v[54:57]
	v_mfma_f32_16x16x32_bf16 v[46:49], v[150:153], v[190:193], v[46:49]
	v_mfma_f32_16x16x32_bf16 v[38:41], v[158:161], v[190:193], v[38:41]
	v_mfma_f32_16x16x32_bf16 v[30:33], v[150:153], v[198:201], v[30:33]
	v_mfma_f32_16x16x32_bf16 v[22:25], v[158:161], v[198:201], v[22:25]
	v_mfma_f32_16x16x32_bf16 v[14:17], v[150:153], v[206:209], v[14:17]
	v_mfma_f32_16x16x32_bf16 v[6:9], v[158:161], v[206:209], v[6:9]
	v_mfma_f32_16x16x32_bf16 v[62:65], v[154:157], v[186:189], v[62:65]
	v_mfma_f32_16x16x32_bf16 v[54:57], v[162:165], v[186:189], v[54:57]
	v_mfma_f32_16x16x32_bf16 v[46:49], v[154:157], v[194:197], v[46:49]
	v_mfma_f32_16x16x32_bf16 v[38:41], v[162:165], v[194:197], v[38:41]
	v_mfma_f32_16x16x32_bf16 v[30:33], v[154:157], v[202:205], v[30:33]
	v_mfma_f32_16x16x32_bf16 v[22:25], v[162:165], v[202:205], v[22:25]
	v_mfma_f32_16x16x32_bf16 v[14:17], v[154:157], v[210:213], v[14:17]
	v_mfma_f32_16x16x32_bf16 v[6:9], v[162:165], v[210:213], v[6:9]
	s_setprio 0
	s_setprio 1
	v_mfma_f32_16x16x32_bf16 v[58:61], v[166:169], v[182:185], v[58:61]
	v_mfma_f32_16x16x32_bf16 v[50:53], v[174:177], v[182:185], v[50:53]
	v_mfma_f32_16x16x32_bf16 v[42:45], v[166:169], v[190:193], v[42:45]
	v_mfma_f32_16x16x32_bf16 v[34:37], v[174:177], v[190:193], v[34:37]
	v_mfma_f32_16x16x32_bf16 v[26:29], v[166:169], v[198:201], v[26:29]
	v_mfma_f32_16x16x32_bf16 v[18:21], v[174:177], v[198:201], v[18:21]
	v_mfma_f32_16x16x32_bf16 v[10:13], v[166:169], v[206:209], v[10:13]
	v_mfma_f32_16x16x32_bf16 v[2:5], v[174:177], v[206:209], v[2:5]
	v_mfma_f32_16x16x32_bf16 v[58:61], v[170:173], v[186:189], v[58:61]
	v_mfma_f32_16x16x32_bf16 v[50:53], v[178:181], v[186:189], v[50:53]
	v_mfma_f32_16x16x32_bf16 v[42:45], v[170:173], v[194:197], v[42:45]
	v_mfma_f32_16x16x32_bf16 v[34:37], v[178:181], v[194:197], v[34:37]
	v_mfma_f32_16x16x32_bf16 v[26:29], v[170:173], v[202:205], v[26:29]
	v_mfma_f32_16x16x32_bf16 v[18:21], v[178:181], v[202:205], v[18:21]
	v_mfma_f32_16x16x32_bf16 v[10:13], v[170:173], v[210:213], v[10:13]
	v_mfma_f32_16x16x32_bf16 v[2:5], v[178:181], v[210:213], v[2:5]
	s_setprio 0
	s_add_i32 s37, s37, 2
	s_add_u32 s27, s27, 0x100
	s_addc_u32 s29, s29, 0
	s_add_u32 s40, s40, 0x100
	s_addc_u32 s41, s41, 0
	s_cmp_gt_u32 s37, 29
	s_barrier
	s_cbranch_scc0 .LBB0_2088
	s_and_b64 vcc, exec, s[22:23]
	s_cbranch_vccz .LBB0_2091
	s_barrier

.LBB0_2272:
	ds_read_b128 v[150:153], v146
	ds_read_b128 v[154:157], v146 offset:1024
	ds_read_b128 v[158:161], v146 offset:2048
	ds_read_b128 v[162:165], v146 offset:3072
	ds_read_b128 v[166:169], v147
	ds_read_b128 v[170:173], v147 offset:1024
	ds_read_b128 v[174:177], v147 offset:2048
	ds_read_b128 v[178:181], v147 offset:3072
	s_add_u32 s2, s30, 0xfffe0080
	s_addc_u32 s3, s31, -1
	s_cmp_eq_u32 s51, 4
	s_cselect_b32 s37, s15, s3
	s_cselect_b32 s36, s48, s2
	s_cselect_b32 s35, s17, s50
	s_cselect_b32 s34, s19, s49
	v_lshl_add_u64 v[142:143], s[30:31], 0, v[140:141]
	s_add_i32 m0, s25, 0xc000
	ds_read_b128 v[182:185], v148
	ds_read_b128 v[186:189], v148 offset:1024
	ds_read_b128 v[190:193], v148 offset:2048
	ds_read_b128 v[194:197], v148 offset:3072
	ds_read_b128 v[198:201], v148 offset:4096
	ds_read_b128 v[202:205], v148 offset:5120
	ds_read_b128 v[206:209], v148 offset:6144
	ds_read_b128 v[210:213], v148 offset:7168
	global_load_lds_dwordx4 v[142:143], off
	v_lshl_add_u64 v[142:143], s[30:31], 0, v[138:139]
	s_add_i32 m0, s25, 0xe000
	s_nop 0
	global_load_lds_dwordx4 v[142:143], off
	s_waitcnt vmcnt(8)
	s_waitcnt lgkmcnt(0)
	s_barrier
	s_setprio 1
	s_waitcnt lgkmcnt(0)
	v_mfma_f32_16x16x32_bf16 v[126:129], v[150:153], v[182:185], v[126:129]
	v_mfma_f32_16x16x32_bf16 v[122:125], v[158:161], v[182:185], v[122:125]
	v_mfma_f32_16x16x32_bf16 v[118:121], v[150:153], v[190:193], v[118:121]
	v_mfma_f32_16x16x32_bf16 v[110:113], v[158:161], v[190:193], v[110:113]
	v_mfma_f32_16x16x32_bf16 v[102:105], v[150:153], v[198:201], v[102:105]
	v_mfma_f32_16x16x32_bf16 v[94:97], v[158:161], v[198:201], v[94:97]
	v_mfma_f32_16x16x32_bf16 v[86:89], v[150:153], v[206:209], v[86:89]
	v_mfma_f32_16x16x32_bf16 v[78:81], v[158:161], v[206:209], v[78:81]
	v_mfma_f32_16x16x32_bf16 v[126:129], v[154:157], v[186:189], v[126:129]
	v_mfma_f32_16x16x32_bf16 v[122:125], v[162:165], v[186:189], v[122:125]
	v_mfma_f32_16x16x32_bf16 v[118:121], v[154:157], v[194:197], v[118:121]
	v_mfma_f32_16x16x32_bf16 v[110:113], v[162:165], v[194:197], v[110:113]
	v_mfma_f32_16x16x32_bf16 v[102:105], v[154:157], v[202:205], v[102:105]
	v_mfma_f32_16x16x32_bf16 v[94:97], v[162:165], v[202:205], v[94:97]
	v_mfma_f32_16x16x32_bf16 v[86:89], v[154:157], v[210:213], v[86:89]
	v_mfma_f32_16x16x32_bf16 v[78:81], v[162:165], v[210:213], v[78:81]
	s_setprio 0
	s_setprio 1
	v_mfma_f32_16x16x32_bf16 v[114:117], v[166:169], v[182:185], v[114:117]
	v_mfma_f32_16x16x32_bf16 v[106:109], v[174:177], v[182:185], v[106:109]
	v_mfma_f32_16x16x32_bf16 v[98:101], v[166:169], v[190:193], v[98:101]
	v_mfma_f32_16x16x32_bf16 v[90:93], v[174:177], v[190:193], v[90:93]
	v_mfma_f32_16x16x32_bf16 v[82:85], v[166:169], v[198:201], v[82:85]
	v_mfma_f32_16x16x32_bf16 v[74:77], v[174:177], v[198:201], v[74:77]
	v_mfma_f32_16x16x32_bf16 v[70:73], v[166:169], v[206:209], v[70:73]
	v_mfma_f32_16x16x32_bf16 v[66:69], v[174:177], v[206:209], v[66:69]
	v_mfma_f32_16x16x32_bf16 v[114:117], v[170:173], v[186:189], v[114:117]
	v_mfma_f32_16x16x32_bf16 v[106:109], v[178:181], v[186:189], v[106:109]
	v_mfma_f32_16x16x32_bf16 v[98:101], v[170:173], v[194:197], v[98:101]
	v_mfma_f32_16x16x32_bf16 v[90:93], v[178:181], v[194:197], v[90:93]
	v_mfma_f32_16x16x32_bf16 v[82:85], v[170:173], v[202:205], v[82:85]
	v_mfma_f32_16x16x32_bf16 v[74:77], v[178:181], v[202:205], v[74:77]
	v_mfma_f32_16x16x32_bf16 v[70:73], v[170:173], v[210:213], v[70:73]
	v_mfma_f32_16x16x32_bf16 v[66:69], v[178:181], v[210:213], v[66:69]
	s_setprio 0
	s_barrier
	s_add_i32 s2, s46, s40
	v_lshl_add_u64 v[142:143], s[34:35], 0, v[134:135]
	s_mov_b32 m0, s2
	ds_read_b128 v[182:185], v148 offset:16384
	ds_read_b128 v[186:189], v148 offset:17408
	ds_read_b128 v[190:193], v148 offset:18432
	ds_read_b128 v[194:197], v148 offset:19456
	ds_read_b128 v[198:201], v148 offset:20480
	ds_read_b128 v[202:205], v148 offset:21504
	ds_read_b128 v[206:209], v148 offset:22528
	ds_read_b128 v[210:213], v148 offset:23552
	global_load_lds_dwordx4 v[142:143], off
	s_add_i32 m0, s2, 0x2000
	s_add_u32 s2, s34, 0x20000
	v_lshl_add_u64 v[214:215], s[34:35], 0, v[130:131]
	s_addc_u32 s3, s35, 0
	s_add_i32 s52, s47, s40
	global_load_lds_dwordx4 v[214:215], off
	v_lshl_add_u64 v[216:217], s[2:3], 0, v[134:135]
	s_mov_b32 m0, s52
	v_lshl_add_u64 v[218:219], s[36:37], 0, v[132:133]
	global_load_lds_dwordx4 v[216:217], off
	v_lshl_add_u64 v[216:217], s[2:3], 0, v[130:131]
	s_add_i32 m0, s52, 0x2000
	s_nop 0
	global_load_lds_dwordx4 v[216:217], off
	v_lshl_add_u64 v[216:217], s[36:37], 0, v[136:137]
	s_mov_b32 m0, s25
	s_nop 0
	global_load_lds_dwordx4 v[216:217], off
	s_mov_b32 m0, s27
	s_nop 0
	global_load_lds_dwordx4 v[218:219], off
	s_waitcnt vmcnt(8)
	s_waitcnt lgkmcnt(0)
	s_barrier
	s_setprio 1
	s_waitcnt lgkmcnt(0)
	v_mfma_f32_16x16x32_bf16 v[62:65], v[150:153], v[182:185], v[62:65]
	v_mfma_f32_16x16x32_bf16 v[58:61], v[158:161], v[182:185], v[58:61]
	v_mfma_f32_16x16x32_bf16 v[54:57], v[150:153], v[190:193], v[54:57]
	v_mfma_f32_16x16x32_bf16 v[46:49], v[158:161], v[190:193], v[46:49]
	v_mfma_f32_16x16x32_bf16 v[38:41], v[150:153], v[198:201], v[38:41]
	v_mfma_f32_16x16x32_bf16 v[30:33], v[158:161], v[198:201], v[30:33]
	v_mfma_f32_16x16x32_bf16 v[22:25], v[150:153], v[206:209], v[22:25]
	v_mfma_f32_16x16x32_bf16 v[14:17], v[158:161], v[206:209], v[14:17]
	v_mfma_f32_16x16x32_bf16 v[62:65], v[154:157], v[186:189], v[62:65]
	v_mfma_f32_16x16x32_bf16 v[58:61], v[162:165], v[186:189], v[58:61]
	v_mfma_f32_16x16x32_bf16 v[54:57], v[154:157], v[194:197], v[54:57]
	v_mfma_f32_16x16x32_bf16 v[46:49], v[162:165], v[194:197], v[46:49]
	v_mfma_f32_16x16x32_bf16 v[38:41], v[154:157], v[202:205], v[38:41]
	v_mfma_f32_16x16x32_bf16 v[30:33], v[162:165], v[202:205], v[30:33]
	v_mfma_f32_16x16x32_bf16 v[22:25], v[154:157], v[210:213], v[22:25]
	v_mfma_f32_16x16x32_bf16 v[14:17], v[162:165], v[210:213], v[14:17]
	s_setprio 0
	s_setprio 1
	v_mfma_f32_16x16x32_bf16 v[50:53], v[166:169], v[182:185], v[50:53]
	v_mfma_f32_16x16x32_bf16 v[42:45], v[174:177], v[182:185], v[42:45]
	v_mfma_f32_16x16x32_bf16 v[34:37], v[166:169], v[190:193], v[34:37]
	v_mfma_f32_16x16x32_bf16 v[26:29], v[174:177], v[190:193], v[26:29]
	v_mfma_f32_16x16x32_bf16 v[18:21], v[166:169], v[198:201], v[18:21]
	v_mfma_f32_16x16x32_bf16 v[10:13], v[174:177], v[198:201], v[10:13]
	v_mfma_f32_16x16x32_bf16 v[6:9], v[166:169], v[206:209], v[6:9]
	v_mfma_f32_16x16x32_bf16 v[2:5], v[174:177], v[206:209], v[2:5]
	v_mfma_f32_16x16x32_bf16 v[50:53], v[170:173], v[186:189], v[50:53]
	v_mfma_f32_16x16x32_bf16 v[42:45], v[178:181], v[186:189], v[42:45]
	v_mfma_f32_16x16x32_bf16 v[34:37], v[170:173], v[194:197], v[34:37]
	v_mfma_f32_16x16x32_bf16 v[26:29], v[178:181], v[194:197], v[26:29]
	v_mfma_f32_16x16x32_bf16 v[18:21], v[170:173], v[202:205], v[18:21]
	v_mfma_f32_16x16x32_bf16 v[10:13], v[178:181], v[202:205], v[10:13]
	v_mfma_f32_16x16x32_bf16 v[6:9], v[170:173], v[210:213], v[6:9]
	v_mfma_f32_16x16x32_bf16 v[2:5], v[178:181], v[210:213], v[2:5]
	s_setprio 0
	s_barrier
	s_add_i32 s52, 0, 0x18000
	v_add_u32_e32 v149, s52, v144
	s_add_i32 s53, 0, 0x1c000
	ds_read_b128 v[150:153], v149
	ds_read_b128 v[154:157], v149 offset:1024
	ds_read_b128 v[158:161], v149 offset:2048
	ds_read_b128 v[162:165], v149 offset:3072
	v_add_u32_e32 v149, s53, v144
	ds_read_b128 v[166:169], v149
	ds_read_b128 v[170:173], v149 offset:1024
	ds_read_b128 v[174:177], v149 offset:2048
	ds_read_b128 v[178:181], v149 offset:3072
	s_add_u32 s2, s36, 0x20000
	s_addc_u32 s3, s37, 0
	s_mov_b32 m0, s41
	v_lshl_add_u64 v[220:221], s[2:3], 0, v[136:137]
	ds_read_b128 v[182:185], v148 offset:32768
	ds_read_b128 v[186:189], v148 offset:33792
	ds_read_b128 v[190:193], v148 offset:34816
	ds_read_b128 v[194:197], v148 offset:35840
	ds_read_b128 v[198:201], v148 offset:36864
	ds_read_b128 v[202:205], v148 offset:37888
	ds_read_b128 v[206:209], v148 offset:38912
	ds_read_b128 v[210:213], v148 offset:39936
	global_load_lds_dwordx4 v[220:221], off
	v_lshl_add_u64 v[220:221], s[2:3], 0, v[132:133]
	s_mov_b32 m0, s42
	s_nop 0
	global_load_lds_dwordx4 v[220:221], off
	s_waitcnt vmcnt(8)
	s_waitcnt lgkmcnt(0)
	s_barrier
	s_setprio 1
	s_waitcnt lgkmcnt(0)
	v_mfma_f32_16x16x32_bf16 v[126:129], v[150:153], v[182:185], v[126:129]
	v_mfma_f32_16x16x32_bf16 v[122:125], v[158:161], v[182:185], v[122:125]
	v_mfma_f32_16x16x32_bf16 v[118:121], v[150:153], v[190:193], v[118:121]
	v_mfma_f32_16x16x32_bf16 v[110:113], v[158:161], v[190:193], v[110:113]
	v_mfma_f32_16x16x32_bf16 v[102:105], v[150:153], v[198:201], v[102:105]
	v_mfma_f32_16x16x32_bf16 v[94:97], v[158:161], v[198:201], v[94:97]
	v_mfma_f32_16x16x32_bf16 v[86:89], v[150:153], v[206:209], v[86:89]
	v_mfma_f32_16x16x32_bf16 v[78:81], v[158:161], v[206:209], v[78:81]
	v_mfma_f32_16x16x32_bf16 v[126:129], v[154:157], v[186:189], v[126:129]
	v_mfma_f32_16x16x32_bf16 v[122:125], v[162:165], v[186:189], v[122:125]
	v_mfma_f32_16x16x32_bf16 v[118:121], v[154:157], v[194:197], v[118:121]
	v_mfma_f32_16x16x32_bf16 v[110:113], v[162:165], v[194:197], v[110:113]
	v_mfma_f32_16x16x32_bf16 v[102:105], v[154:157], v[202:205], v[102:105]
	v_mfma_f32_16x16x32_bf16 v[94:97], v[162:165], v[202:205], v[94:97]
	v_mfma_f32_16x16x32_bf16 v[86:89], v[154:157], v[210:213], v[86:89]
	v_mfma_f32_16x16x32_bf16 v[78:81], v[162:165], v[210:213], v[78:81]
	s_setprio 0
	s_setprio 1
	v_mfma_f32_16x16x32_bf16 v[114:117], v[166:169], v[182:185], v[114:117]
	v_mfma_f32_16x16x32_bf16 v[106:109], v[174:177], v[182:185], v[106:109]
	v_mfma_f32_16x16x32_bf16 v[98:101], v[166:169], v[190:193], v[98:101]
	v_mfma_f32_16x16x32_bf16 v[90:93], v[174:177], v[190:193], v[90:93]
	v_mfma_f32_16x16x32_bf16 v[82:85], v[166:169], v[198:201], v[82:85]
	v_mfma_f32_16x16x32_bf16 v[74:77], v[174:177], v[198:201], v[74:77]
	v_mfma_f32_16x16x32_bf16 v[70:73], v[166:169], v[206:209], v[70:73]
	v_mfma_f32_16x16x32_bf16 v[66:69], v[174:177], v[206:209], v[66:69]
	v_mfma_f32_16x16x32_bf16 v[114:117], v[170:173], v[186:189], v[114:117]
	v_mfma_f32_16x16x32_bf16 v[106:109], v[178:181], v[186:189], v[106:109]
	v_mfma_f32_16x16x32_bf16 v[98:101], v[170:173], v[194:197], v[98:101]
	v_mfma_f32_16x16x32_bf16 v[90:93], v[178:181], v[194:197], v[90:93]
	v_mfma_f32_16x16x32_bf16 v[82:85], v[170:173], v[202:205], v[82:85]
	v_mfma_f32_16x16x32_bf16 v[74:77], v[178:181], v[202:205], v[74:77]
	v_mfma_f32_16x16x32_bf16 v[70:73], v[170:173], v[210:213], v[70:73]
	v_mfma_f32_16x16x32_bf16 v[66:69], v[178:181], v[210:213], v[66:69]
	s_setprio 0
	s_barrier
	s_add_i32 s2, s52, s40
	v_lshl_add_u64 v[142:143], v[142:143], 0, s[6:7]
	s_mov_b32 m0, s2
	ds_read_b128 v[182:185], v148 offset:49152
	ds_read_b128 v[186:189], v148 offset:50176
	ds_read_b128 v[190:193], v148 offset:51200
	ds_read_b128 v[194:197], v148 offset:52224
	ds_read_b128 v[198:201], v148 offset:53248
	ds_read_b128 v[202:205], v148 offset:54272
	ds_read_b128 v[206:209], v148 offset:55296
	ds_read_b128 v[210:213], v148 offset:56320
	global_load_lds_dwordx4 v[142:143], off
	s_add_i32 m0, s2, 0x2000
	s_add_u32 s2, s34, 0x20080
	v_lshl_add_u64 v[142:143], v[214:215], 0, s[6:7]
	s_addc_u32 s3, s35, 0
	s_add_i32 s34, s53, s40
	global_load_lds_dwordx4 v[142:143], off
	v_lshl_add_u64 v[142:143], s[2:3], 0, v[134:135]
	s_mov_b32 m0, s34
	s_nop 0
	global_load_lds_dwordx4 v[142:143], off
	v_lshl_add_u64 v[142:143], s[2:3], 0, v[130:131]
	s_add_i32 m0, s34, 0x2000
	s_nop 0
	global_load_lds_dwordx4 v[142:143], off
	v_lshl_add_u64 v[142:143], v[216:217], 0, s[6:7]
	s_mov_b32 m0, s44
	s_nop 0
	global_load_lds_dwordx4 v[142:143], off
	v_lshl_add_u64 v[142:143], v[218:219], 0, s[6:7]
	s_mov_b32 m0, s45
	s_nop 0
	global_load_lds_dwordx4 v[142:143], off
	s_waitcnt vmcnt(8)
	s_waitcnt lgkmcnt(0)
	s_barrier
	s_setprio 1
	s_waitcnt lgkmcnt(0)
	v_mfma_f32_16x16x32_bf16 v[62:65], v[150:153], v[182:185], v[62:65]
	v_mfma_f32_16x16x32_bf16 v[58:61], v[158:161], v[182:185], v[58:61]
	v_mfma_f32_16x16x32_bf16 v[54:57], v[150:153], v[190:193], v[54:57]
	v_mfma_f32_16x16x32_bf16 v[46:49], v[158:161], v[190:193], v[46:49]
	v_mfma_f32_16x16x32_bf16 v[38:41], v[150:153], v[198:201], v[38:41]
	v_mfma_f32_16x16x32_bf16 v[30:33], v[158:161], v[198:201], v[30:33]
	v_mfma_f32_16x16x32_bf16 v[22:25], v[150:153], v[206:209], v[22:25]
	v_mfma_f32_16x16x32_bf16 v[14:17], v[158:161], v[206:209], v[14:17]
	v_mfma_f32_16x16x32_bf16 v[62:65], v[154:157], v[186:189], v[62:65]
	v_mfma_f32_16x16x32_bf16 v[58:61], v[162:165], v[186:189], v[58:61]
	v_mfma_f32_16x16x32_bf16 v[54:57], v[154:157], v[194:197], v[54:57]
	v_mfma_f32_16x16x32_bf16 v[46:49], v[162:165], v[194:197], v[46:49]
	v_mfma_f32_16x16x32_bf16 v[38:41], v[154:157], v[202:205], v[38:41]
	v_mfma_f32_16x16x32_bf16 v[30:33], v[162:165], v[202:205], v[30:33]
	v_mfma_f32_16x16x32_bf16 v[22:25], v[154:157], v[210:213], v[22:25]
	v_mfma_f32_16x16x32_bf16 v[14:17], v[162:165], v[210:213], v[14:17]
	s_setprio 0
	s_setprio 1
	v_mfma_f32_16x16x32_bf16 v[50:53], v[166:169], v[182:185], v[50:53]
	v_mfma_f32_16x16x32_bf16 v[42:45], v[174:177], v[182:185], v[42:45]
	v_mfma_f32_16x16x32_bf16 v[34:37], v[166:169], v[190:193], v[34:37]
	v_mfma_f32_16x16x32_bf16 v[26:29], v[174:177], v[190:193], v[26:29]
	v_mfma_f32_16x16x32_bf16 v[18:21], v[166:169], v[198:201], v[18:21]
	v_mfma_f32_16x16x32_bf16 v[10:13], v[174:177], v[198:201], v[10:13]
	v_mfma_f32_16x16x32_bf16 v[6:9], v[166:169], v[206:209], v[6:9]
	v_mfma_f32_16x16x32_bf16 v[2:5], v[174:177], v[206:209], v[2:5]
	v_mfma_f32_16x16x32_bf16 v[50:53], v[170:173], v[186:189], v[50:53]
	v_mfma_f32_16x16x32_bf16 v[42:45], v[178:181], v[186:189], v[42:45]
	v_mfma_f32_16x16x32_bf16 v[34:37], v[170:173], v[194:197], v[34:37]
	v_mfma_f32_16x16x32_bf16 v[26:29], v[178:181], v[194:197], v[26:29]
	v_mfma_f32_16x16x32_bf16 v[18:21], v[170:173], v[202:205], v[18:21]
	v_mfma_f32_16x16x32_bf16 v[10:13], v[178:181], v[202:205], v[10:13]
	v_mfma_f32_16x16x32_bf16 v[6:9], v[170:173], v[210:213], v[6:9]
	v_mfma_f32_16x16x32_bf16 v[2:5], v[178:181], v[210:213], v[2:5]
	s_setprio 0
	s_add_i32 s51, s51, 2
	s_add_u32 s49, s49, 0x100
	s_addc_u32 s50, s50, 0
	s_add_u32 s30, s30, 0x100
	s_addc_u32 s31, s31, 0
	s_cmp_gt_u32 s51, 5
	s_barrier
	s_cbranch_scc0 .LBB0_2272
	s_and_b64 vcc, exec, s[12:13]
	s_cbranch_vccz .LBB0_2275
	s_barrier

.LBB0_2545:
	ds_read_b128 v[130:133], v159
	ds_read_b128 v[134:137], v159 offset:1024
	ds_read_b128 v[162:165], v159 offset:2048
	ds_read_b128 v[166:169], v159 offset:3072
	ds_read_b128 v[170:173], v160
	ds_read_b128 v[174:177], v160 offset:1024
	ds_read_b128 v[178:181], v160 offset:2048
	ds_read_b128 v[182:185], v160 offset:3072
	s_add_u32 s2, s36, 0xfff80080
	s_addc_u32 s3, s37, -1
	s_cmp_eq_u32 s55, 28
	s_cselect_b32 s41, s21, s3
	s_cselect_b32 s40, s31, s2
	s_cselect_b32 s39, s23, s54
	s_cselect_b32 s38, s35, s53
	v_lshl_add_u64 v[138:139], s[36:37], 0, v[152:153]
	s_add_i32 m0, s43, 0xc000
	ds_read_b128 v[186:189], v161
	ds_read_b128 v[190:193], v161 offset:1024
	ds_read_b128 v[194:197], v161 offset:2048
	ds_read_b128 v[198:201], v161 offset:3072
	ds_read_b128 v[202:205], v161 offset:4096
	ds_read_b128 v[206:209], v161 offset:5120
	ds_read_b128 v[210:213], v161 offset:6144
	ds_read_b128 v[214:217], v161 offset:7168
	global_load_lds_dwordx4 v[138:139], off
	v_lshl_add_u64 v[138:139], s[36:37], 0, v[150:151]
	s_add_i32 m0, s43, 0xe000
	s_nop 0
	global_load_lds_dwordx4 v[138:139], off
	s_waitcnt vmcnt(8)
	s_waitcnt lgkmcnt(0)
	s_barrier
	s_setprio 1
	s_waitcnt lgkmcnt(0)
	v_mfma_f32_16x16x32_bf16 v[126:129], v[130:133], v[186:189], v[126:129]
	v_mfma_f32_16x16x32_bf16 v[122:125], v[162:165], v[186:189], v[122:125]
	v_mfma_f32_16x16x32_bf16 v[110:113], v[130:133], v[194:197], v[110:113]
	v_mfma_f32_16x16x32_bf16 v[106:109], v[162:165], v[194:197], v[106:109]
	v_mfma_f32_16x16x32_bf16 v[94:97], v[130:133], v[202:205], v[94:97]
	v_mfma_f32_16x16x32_bf16 v[90:93], v[162:165], v[202:205], v[90:93]
	v_mfma_f32_16x16x32_bf16 v[78:81], v[130:133], v[210:213], v[78:81]
	v_mfma_f32_16x16x32_bf16 v[74:77], v[162:165], v[210:213], v[74:77]
	v_mfma_f32_16x16x32_bf16 v[126:129], v[134:137], v[190:193], v[126:129]
	v_mfma_f32_16x16x32_bf16 v[122:125], v[166:169], v[190:193], v[122:125]
	v_mfma_f32_16x16x32_bf16 v[110:113], v[134:137], v[198:201], v[110:113]
	v_mfma_f32_16x16x32_bf16 v[106:109], v[166:169], v[198:201], v[106:109]
	v_mfma_f32_16x16x32_bf16 v[94:97], v[134:137], v[206:209], v[94:97]
	v_mfma_f32_16x16x32_bf16 v[90:93], v[166:169], v[206:209], v[90:93]
	v_mfma_f32_16x16x32_bf16 v[78:81], v[134:137], v[214:217], v[78:81]
	v_mfma_f32_16x16x32_bf16 v[74:77], v[166:169], v[214:217], v[74:77]
	s_setprio 0
	s_setprio 1
	v_mfma_f32_16x16x32_bf16 v[118:121], v[170:173], v[186:189], v[118:121]
	v_mfma_f32_16x16x32_bf16 v[114:117], v[178:181], v[186:189], v[114:117]
	v_mfma_f32_16x16x32_bf16 v[102:105], v[170:173], v[194:197], v[102:105]
	v_mfma_f32_16x16x32_bf16 v[98:101], v[178:181], v[194:197], v[98:101]
	v_mfma_f32_16x16x32_bf16 v[86:89], v[170:173], v[202:205], v[86:89]
	v_mfma_f32_16x16x32_bf16 v[82:85], v[178:181], v[202:205], v[82:85]
	v_mfma_f32_16x16x32_bf16 v[70:73], v[170:173], v[210:213], v[70:73]
	v_mfma_f32_16x16x32_bf16 v[66:69], v[178:181], v[210:213], v[66:69]
	v_mfma_f32_16x16x32_bf16 v[118:121], v[174:177], v[190:193], v[118:121]
	v_mfma_f32_16x16x32_bf16 v[114:117], v[182:185], v[190:193], v[114:117]
	v_mfma_f32_16x16x32_bf16 v[102:105], v[174:177], v[198:201], v[102:105]
	v_mfma_f32_16x16x32_bf16 v[98:101], v[182:185], v[198:201], v[98:101]
	v_mfma_f32_16x16x32_bf16 v[86:89], v[174:177], v[206:209], v[86:89]
	v_mfma_f32_16x16x32_bf16 v[82:85], v[182:185], v[206:209], v[82:85]
	v_mfma_f32_16x16x32_bf16 v[70:73], v[174:177], v[214:217], v[70:73]
	v_mfma_f32_16x16x32_bf16 v[66:69], v[182:185], v[214:217], v[66:69]
	s_setprio 0
	s_barrier
	s_add_i32 s2, s50, s42
	v_lshl_add_u64 v[138:139], s[38:39], 0, v[142:143]
	s_mov_b32 m0, s2
	ds_read_b128 v[186:189], v161 offset:16384
	ds_read_b128 v[190:193], v161 offset:17408
	ds_read_b128 v[194:197], v161 offset:18432
	ds_read_b128 v[198:201], v161 offset:19456
	ds_read_b128 v[202:205], v161 offset:20480
	ds_read_b128 v[206:209], v161 offset:21504
	ds_read_b128 v[210:213], v161 offset:22528
	ds_read_b128 v[214:217], v161 offset:23552
	global_load_lds_dwordx4 v[138:139], off
	s_add_i32 m0, s2, 0x2000
	s_add_u32 s2, s38, 0x80000
	v_lshl_add_u64 v[154:155], s[38:39], 0, v[146:147]
	s_addc_u32 s3, s39, 0
	s_add_i32 s56, s51, s42
	global_load_lds_dwordx4 v[154:155], off
	v_lshl_add_u64 v[218:219], s[2:3], 0, v[142:143]
	s_mov_b32 m0, s56
	v_lshl_add_u64 v[220:221], s[40:41], 0, v[144:145]
	global_load_lds_dwordx4 v[218:219], off
	v_lshl_add_u64 v[218:219], s[2:3], 0, v[146:147]
	s_add_i32 m0, s56, 0x2000
	s_nop 0
	global_load_lds_dwordx4 v[218:219], off
	v_lshl_add_u64 v[218:219], s[40:41], 0, v[140:141]
	s_mov_b32 m0, s43
	s_nop 0
	global_load_lds_dwordx4 v[218:219], off
	s_mov_b32 m0, s44
	s_nop 0
	global_load_lds_dwordx4 v[220:221], off
	s_waitcnt vmcnt(8)
	s_waitcnt lgkmcnt(0)
	s_barrier
	s_setprio 1
	s_waitcnt lgkmcnt(0)
	v_mfma_f32_16x16x32_bf16 v[62:65], v[130:133], v[186:189], v[62:65]
	v_mfma_f32_16x16x32_bf16 v[58:61], v[162:165], v[186:189], v[58:61]
	v_mfma_f32_16x16x32_bf16 v[46:49], v[130:133], v[194:197], v[46:49]
	v_mfma_f32_16x16x32_bf16 v[42:45], v[162:165], v[194:197], v[42:45]
	v_mfma_f32_16x16x32_bf16 v[30:33], v[130:133], v[202:205], v[30:33]
	v_mfma_f32_16x16x32_bf16 v[26:29], v[162:165], v[202:205], v[26:29]
	v_mfma_f32_16x16x32_bf16 v[14:17], v[130:133], v[210:213], v[14:17]
	v_mfma_f32_16x16x32_bf16 v[10:13], v[162:165], v[210:213], v[10:13]
	v_mfma_f32_16x16x32_bf16 v[62:65], v[134:137], v[190:193], v[62:65]
	v_mfma_f32_16x16x32_bf16 v[58:61], v[166:169], v[190:193], v[58:61]
	v_mfma_f32_16x16x32_bf16 v[46:49], v[134:137], v[198:201], v[46:49]
	v_mfma_f32_16x16x32_bf16 v[42:45], v[166:169], v[198:201], v[42:45]
	v_mfma_f32_16x16x32_bf16 v[30:33], v[134:137], v[206:209], v[30:33]
	v_mfma_f32_16x16x32_bf16 v[26:29], v[166:169], v[206:209], v[26:29]
	v_mfma_f32_16x16x32_bf16 v[14:17], v[134:137], v[214:217], v[14:17]
	v_mfma_f32_16x16x32_bf16 v[10:13], v[166:169], v[214:217], v[10:13]
	s_setprio 0
	s_setprio 1
	v_mfma_f32_16x16x32_bf16 v[54:57], v[170:173], v[186:189], v[54:57]
	v_mfma_f32_16x16x32_bf16 v[50:53], v[178:181], v[186:189], v[50:53]
	v_mfma_f32_16x16x32_bf16 v[38:41], v[170:173], v[194:197], v[38:41]
	v_mfma_f32_16x16x32_bf16 v[34:37], v[178:181], v[194:197], v[34:37]
	v_mfma_f32_16x16x32_bf16 v[22:25], v[170:173], v[202:205], v[22:25]
	v_mfma_f32_16x16x32_bf16 v[18:21], v[178:181], v[202:205], v[18:21]
	v_mfma_f32_16x16x32_bf16 v[6:9], v[170:173], v[210:213], v[6:9]
	v_mfma_f32_16x16x32_bf16 v[2:5], v[178:181], v[210:213], v[2:5]
	v_mfma_f32_16x16x32_bf16 v[54:57], v[174:177], v[190:193], v[54:57]
	v_mfma_f32_16x16x32_bf16 v[50:53], v[182:185], v[190:193], v[50:53]
	v_mfma_f32_16x16x32_bf16 v[38:41], v[174:177], v[198:201], v[38:41]
	v_mfma_f32_16x16x32_bf16 v[34:37], v[182:185], v[198:201], v[34:37]
	v_mfma_f32_16x16x32_bf16 v[22:25], v[174:177], v[206:209], v[22:25]
	v_mfma_f32_16x16x32_bf16 v[18:21], v[182:185], v[206:209], v[18:21]
	v_mfma_f32_16x16x32_bf16 v[6:9], v[174:177], v[214:217], v[6:9]
	v_mfma_f32_16x16x32_bf16 v[2:5], v[182:185], v[214:217], v[2:5]
	s_setprio 0
	s_barrier
	s_add_i32 s56, 0, 0x18000
	v_add_u32_e32 v148, s56, v157
	s_add_i32 s57, 0, 0x1c000
	ds_read_b128 v[130:133], v148
	ds_read_b128 v[134:137], v148 offset:1024
	ds_read_b128 v[162:165], v148 offset:2048
	ds_read_b128 v[166:169], v148 offset:3072
	v_add_u32_e32 v148, s57, v157
	ds_read_b128 v[170:173], v148
	ds_read_b128 v[174:177], v148 offset:1024
	ds_read_b128 v[178:181], v148 offset:2048
	ds_read_b128 v[182:185], v148 offset:3072
	s_add_u32 s2, s40, 0x80000
	s_addc_u32 s3, s41, 0
	s_mov_b32 m0, s45
	v_lshl_add_u64 v[222:223], s[2:3], 0, v[140:141]
	ds_read_b128 v[186:189], v161 offset:32768
	ds_read_b128 v[190:193], v161 offset:33792
	ds_read_b128 v[194:197], v161 offset:34816
	ds_read_b128 v[198:201], v161 offset:35840
	ds_read_b128 v[202:205], v161 offset:36864
	ds_read_b128 v[206:209], v161 offset:37888
	ds_read_b128 v[210:213], v161 offset:38912
	ds_read_b128 v[214:217], v161 offset:39936
	global_load_lds_dwordx4 v[222:223], off
	v_lshl_add_u64 v[222:223], s[2:3], 0, v[144:145]
	s_mov_b32 m0, s46
	s_nop 0
	global_load_lds_dwordx4 v[222:223], off
	s_waitcnt vmcnt(8)
	s_waitcnt lgkmcnt(0)
	s_barrier
	s_setprio 1
	s_waitcnt lgkmcnt(0)
	v_mfma_f32_16x16x32_bf16 v[126:129], v[130:133], v[186:189], v[126:129]
	v_mfma_f32_16x16x32_bf16 v[122:125], v[162:165], v[186:189], v[122:125]
	v_mfma_f32_16x16x32_bf16 v[110:113], v[130:133], v[194:197], v[110:113]
	v_mfma_f32_16x16x32_bf16 v[106:109], v[162:165], v[194:197], v[106:109]
	v_mfma_f32_16x16x32_bf16 v[94:97], v[130:133], v[202:205], v[94:97]
	v_mfma_f32_16x16x32_bf16 v[90:93], v[162:165], v[202:205], v[90:93]
	v_mfma_f32_16x16x32_bf16 v[78:81], v[130:133], v[210:213], v[78:81]
	v_mfma_f32_16x16x32_bf16 v[74:77], v[162:165], v[210:213], v[74:77]
	v_mfma_f32_16x16x32_bf16 v[126:129], v[134:137], v[190:193], v[126:129]
	v_mfma_f32_16x16x32_bf16 v[122:125], v[166:169], v[190:193], v[122:125]
	v_mfma_f32_16x16x32_bf16 v[110:113], v[134:137], v[198:201], v[110:113]
	v_mfma_f32_16x16x32_bf16 v[106:109], v[166:169], v[198:201], v[106:109]
	v_mfma_f32_16x16x32_bf16 v[94:97], v[134:137], v[206:209], v[94:97]
	v_mfma_f32_16x16x32_bf16 v[90:93], v[166:169], v[206:209], v[90:93]
	v_mfma_f32_16x16x32_bf16 v[78:81], v[134:137], v[214:217], v[78:81]
	v_mfma_f32_16x16x32_bf16 v[74:77], v[166:169], v[214:217], v[74:77]
	s_setprio 0
	s_setprio 1
	v_mfma_f32_16x16x32_bf16 v[118:121], v[170:173], v[186:189], v[118:121]
	v_mfma_f32_16x16x32_bf16 v[114:117], v[178:181], v[186:189], v[114:117]
	v_mfma_f32_16x16x32_bf16 v[102:105], v[170:173], v[194:197], v[102:105]
	v_mfma_f32_16x16x32_bf16 v[98:101], v[178:181], v[194:197], v[98:101]
	v_mfma_f32_16x16x32_bf16 v[86:89], v[170:173], v[202:205], v[86:89]
	v_mfma_f32_16x16x32_bf16 v[82:85], v[178:181], v[202:205], v[82:85]
	v_mfma_f32_16x16x32_bf16 v[70:73], v[170:173], v[210:213], v[70:73]
	v_mfma_f32_16x16x32_bf16 v[66:69], v[178:181], v[210:213], v[66:69]
	v_mfma_f32_16x16x32_bf16 v[118:121], v[174:177], v[190:193], v[118:121]
	v_mfma_f32_16x16x32_bf16 v[114:117], v[182:185], v[190:193], v[114:117]
	v_mfma_f32_16x16x32_bf16 v[102:105], v[174:177], v[198:201], v[102:105]
	v_mfma_f32_16x16x32_bf16 v[98:101], v[182:185], v[198:201], v[98:101]
	v_mfma_f32_16x16x32_bf16 v[86:89], v[174:177], v[206:209], v[86:89]
	v_mfma_f32_16x16x32_bf16 v[82:85], v[182:185], v[206:209], v[82:85]
	v_mfma_f32_16x16x32_bf16 v[70:73], v[174:177], v[214:217], v[70:73]
	v_mfma_f32_16x16x32_bf16 v[66:69], v[182:185], v[214:217], v[66:69]
	s_setprio 0
	s_barrier
	s_add_i32 s2, s56, s42
	v_lshl_add_u64 v[138:139], v[138:139], 0, s[16:17]
	s_mov_b32 m0, s2
	ds_read_b128 v[186:189], v161 offset:49152
	ds_read_b128 v[190:193], v161 offset:50176
	ds_read_b128 v[194:197], v161 offset:51200
	ds_read_b128 v[198:201], v161 offset:52224
	ds_read_b128 v[202:205], v161 offset:53248
	ds_read_b128 v[206:209], v161 offset:54272
	ds_read_b128 v[210:213], v161 offset:55296
	ds_read_b128 v[214:217], v161 offset:56320
	global_load_lds_dwordx4 v[138:139], off
	s_add_i32 m0, s2, 0x2000
	s_add_u32 s2, s38, 0x80080
	v_lshl_add_u64 v[138:139], v[154:155], 0, s[16:17]
	s_addc_u32 s3, s39, 0
	s_add_i32 s38, s57, s42
	global_load_lds_dwordx4 v[138:139], off
	v_lshl_add_u64 v[138:139], s[2:3], 0, v[142:143]
	s_mov_b32 m0, s38
	s_nop 0
	global_load_lds_dwordx4 v[138:139], off
	v_lshl_add_u64 v[138:139], s[2:3], 0, v[146:147]
	s_add_i32 m0, s38, 0x2000
	s_nop 0
	global_load_lds_dwordx4 v[138:139], off
	v_lshl_add_u64 v[138:139], v[218:219], 0, s[16:17]
	s_mov_b32 m0, s48
	s_nop 0
	global_load_lds_dwordx4 v[138:139], off
	v_lshl_add_u64 v[138:139], v[220:221], 0, s[16:17]
	s_mov_b32 m0, s49
	s_nop 0
	global_load_lds_dwordx4 v[138:139], off
	s_waitcnt vmcnt(8)
	s_waitcnt lgkmcnt(0)
	s_barrier
	s_setprio 1
	s_waitcnt lgkmcnt(0)
	v_mfma_f32_16x16x32_bf16 v[62:65], v[130:133], v[186:189], v[62:65]
	v_mfma_f32_16x16x32_bf16 v[58:61], v[162:165], v[186:189], v[58:61]
	v_mfma_f32_16x16x32_bf16 v[46:49], v[130:133], v[194:197], v[46:49]
	v_mfma_f32_16x16x32_bf16 v[42:45], v[162:165], v[194:197], v[42:45]
	v_mfma_f32_16x16x32_bf16 v[30:33], v[130:133], v[202:205], v[30:33]
	v_mfma_f32_16x16x32_bf16 v[26:29], v[162:165], v[202:205], v[26:29]
	v_mfma_f32_16x16x32_bf16 v[14:17], v[130:133], v[210:213], v[14:17]
	v_mfma_f32_16x16x32_bf16 v[10:13], v[162:165], v[210:213], v[10:13]
	v_mfma_f32_16x16x32_bf16 v[62:65], v[134:137], v[190:193], v[62:65]
	v_mfma_f32_16x16x32_bf16 v[58:61], v[166:169], v[190:193], v[58:61]
	v_mfma_f32_16x16x32_bf16 v[46:49], v[134:137], v[198:201], v[46:49]
	v_mfma_f32_16x16x32_bf16 v[42:45], v[166:169], v[198:201], v[42:45]
	v_mfma_f32_16x16x32_bf16 v[30:33], v[134:137], v[206:209], v[30:33]
	v_mfma_f32_16x16x32_bf16 v[26:29], v[166:169], v[206:209], v[26:29]
	v_mfma_f32_16x16x32_bf16 v[14:17], v[134:137], v[214:217], v[14:17]
	v_mfma_f32_16x16x32_bf16 v[10:13], v[166:169], v[214:217], v[10:13]
	s_setprio 0
	s_setprio 1
	v_mfma_f32_16x16x32_bf16 v[54:57], v[170:173], v[186:189], v[54:57]
	v_mfma_f32_16x16x32_bf16 v[50:53], v[178:181], v[186:189], v[50:53]
	v_mfma_f32_16x16x32_bf16 v[38:41], v[170:173], v[194:197], v[38:41]
	v_mfma_f32_16x16x32_bf16 v[34:37], v[178:181], v[194:197], v[34:37]
	v_mfma_f32_16x16x32_bf16 v[22:25], v[170:173], v[202:205], v[22:25]
	v_mfma_f32_16x16x32_bf16 v[18:21], v[178:181], v[202:205], v[18:21]
	v_mfma_f32_16x16x32_bf16 v[6:9], v[170:173], v[210:213], v[6:9]
	v_mfma_f32_16x16x32_bf16 v[2:5], v[178:181], v[210:213], v[2:5]
	v_mfma_f32_16x16x32_bf16 v[54:57], v[174:177], v[190:193], v[54:57]
	v_mfma_f32_16x16x32_bf16 v[50:53], v[182:185], v[190:193], v[50:53]
	v_mfma_f32_16x16x32_bf16 v[38:41], v[174:177], v[198:201], v[38:41]
	v_mfma_f32_16x16x32_bf16 v[34:37], v[182:185], v[198:201], v[34:37]
	v_mfma_f32_16x16x32_bf16 v[22:25], v[174:177], v[206:209], v[22:25]
	v_mfma_f32_16x16x32_bf16 v[18:21], v[182:185], v[206:209], v[18:21]
	v_mfma_f32_16x16x32_bf16 v[6:9], v[174:177], v[214:217], v[6:9]
	v_mfma_f32_16x16x32_bf16 v[2:5], v[182:185], v[214:217], v[2:5]
	s_setprio 0
	s_add_i32 s55, s55, 2
	s_add_u32 s53, s53, 0x100
	s_addc_u32 s54, s54, 0
	s_add_u32 s36, s36, 0x100
	s_addc_u32 s37, s37, 0
	s_cmp_gt_u32 s55, 29
	s_barrier
	s_cbranch_scc0 .LBB0_2545
	s_and_b64 vcc, exec, s[18:19]
	s_cbranch_vccz .LBB0_2548
	s_barrier

.LBB0_3799:
	ds_read_b128 v[144:147], v162
	ds_read_b128 v[148:151], v162 offset:1024
	ds_read_b128 v[152:155], v162 offset:2048
	ds_read_b128 v[156:159], v162 offset:3072
	ds_read_b128 v[166:169], v163
	ds_read_b128 v[170:173], v163 offset:1024
	ds_read_b128 v[174:177], v163 offset:2048
	ds_read_b128 v[178:181], v163 offset:3072
	s_add_u32 s2, s40, 0xfff80080
	s_addc_u32 s3, s41, -1
	s_cmp_eq_u32 s58, 28
	s_cselect_b32 s45, s7, s3
	s_cselect_b32 s44, s29, s2
	s_cselect_b32 s43, s31, s57
	s_cselect_b32 s42, s39, s56
	v_lshl_add_u64 v[214:215], s[40:41], 0, v[142:143]
	s_add_i32 m0, s9, 0xc000
	ds_read_b128 v[182:185], v164
	ds_read_b128 v[186:189], v164 offset:1024
	ds_read_b128 v[190:193], v164 offset:2048
	ds_read_b128 v[194:197], v164 offset:3072
	ds_read_b128 v[198:201], v164 offset:4096
	ds_read_b128 v[202:205], v164 offset:5120
	ds_read_b128 v[206:209], v164 offset:6144
	ds_read_b128 v[210:213], v164 offset:7168
	global_load_lds_dwordx4 v[214:215], off
	v_lshl_add_u64 v[214:215], s[40:41], 0, v[140:141]
	s_add_i32 m0, s9, 0xe000
	s_nop 0
	global_load_lds_dwordx4 v[214:215], off
	s_waitcnt vmcnt(8)
	s_waitcnt lgkmcnt(0)
	s_barrier
	s_setprio 1
	s_waitcnt lgkmcnt(0)
	v_mfma_f32_16x16x32_bf16 v[126:129], v[144:147], v[182:185], v[126:129]
	v_mfma_f32_16x16x32_bf16 v[122:125], v[152:155], v[182:185], v[122:125]
	v_mfma_f32_16x16x32_bf16 v[110:113], v[144:147], v[190:193], v[110:113]
	v_mfma_f32_16x16x32_bf16 v[106:109], v[152:155], v[190:193], v[106:109]
	v_mfma_f32_16x16x32_bf16 v[94:97], v[144:147], v[198:201], v[94:97]
	v_mfma_f32_16x16x32_bf16 v[90:93], v[152:155], v[198:201], v[90:93]
	v_mfma_f32_16x16x32_bf16 v[78:81], v[144:147], v[206:209], v[78:81]
	v_mfma_f32_16x16x32_bf16 v[74:77], v[152:155], v[206:209], v[74:77]
	v_mfma_f32_16x16x32_bf16 v[126:129], v[148:151], v[186:189], v[126:129]
	v_mfma_f32_16x16x32_bf16 v[122:125], v[156:159], v[186:189], v[122:125]
	v_mfma_f32_16x16x32_bf16 v[110:113], v[148:151], v[194:197], v[110:113]
	v_mfma_f32_16x16x32_bf16 v[106:109], v[156:159], v[194:197], v[106:109]
	v_mfma_f32_16x16x32_bf16 v[94:97], v[148:151], v[202:205], v[94:97]
	v_mfma_f32_16x16x32_bf16 v[90:93], v[156:159], v[202:205], v[90:93]
	v_mfma_f32_16x16x32_bf16 v[78:81], v[148:151], v[210:213], v[78:81]
	v_mfma_f32_16x16x32_bf16 v[74:77], v[156:159], v[210:213], v[74:77]
	s_setprio 0
	s_setprio 1
	v_mfma_f32_16x16x32_bf16 v[118:121], v[166:169], v[182:185], v[118:121]
	v_mfma_f32_16x16x32_bf16 v[114:117], v[174:177], v[182:185], v[114:117]
	v_mfma_f32_16x16x32_bf16 v[102:105], v[166:169], v[190:193], v[102:105]
	v_mfma_f32_16x16x32_bf16 v[98:101], v[174:177], v[190:193], v[98:101]
	v_mfma_f32_16x16x32_bf16 v[86:89], v[166:169], v[198:201], v[86:89]
	v_mfma_f32_16x16x32_bf16 v[82:85], v[174:177], v[198:201], v[82:85]
	v_mfma_f32_16x16x32_bf16 v[70:73], v[166:169], v[206:209], v[70:73]
	v_mfma_f32_16x16x32_bf16 v[66:69], v[174:177], v[206:209], v[66:69]
	v_mfma_f32_16x16x32_bf16 v[118:121], v[170:173], v[186:189], v[118:121]
	v_mfma_f32_16x16x32_bf16 v[114:117], v[178:181], v[186:189], v[114:117]
	v_mfma_f32_16x16x32_bf16 v[102:105], v[170:173], v[194:197], v[102:105]
	v_mfma_f32_16x16x32_bf16 v[98:101], v[178:181], v[194:197], v[98:101]
	v_mfma_f32_16x16x32_bf16 v[86:89], v[170:173], v[202:205], v[86:89]
	v_mfma_f32_16x16x32_bf16 v[82:85], v[178:181], v[202:205], v[82:85]
	v_mfma_f32_16x16x32_bf16 v[70:73], v[170:173], v[210:213], v[70:73]
	v_mfma_f32_16x16x32_bf16 v[66:69], v[178:181], v[210:213], v[66:69]
	s_setprio 0
	s_barrier
	s_add_i32 s2, s54, s8
	v_lshl_add_u64 v[214:215], s[42:43], 0, v[132:133]
	s_mov_b32 m0, s2
	ds_read_b128 v[182:185], v164 offset:16384
	ds_read_b128 v[186:189], v164 offset:17408
	ds_read_b128 v[190:193], v164 offset:18432
	ds_read_b128 v[194:197], v164 offset:19456
	ds_read_b128 v[198:201], v164 offset:20480
	ds_read_b128 v[202:205], v164 offset:21504
	ds_read_b128 v[206:209], v164 offset:22528
	ds_read_b128 v[210:213], v164 offset:23552
	global_load_lds_dwordx4 v[214:215], off
	s_add_i32 m0, s2, 0x2000
	s_add_u32 s2, s42, 0x80000
	v_lshl_add_u64 v[216:217], s[42:43], 0, v[136:137]
	s_addc_u32 s3, s43, 0
	s_add_i32 s59, s55, s8
	global_load_lds_dwordx4 v[216:217], off
	v_lshl_add_u64 v[218:219], s[2:3], 0, v[132:133]
	s_mov_b32 m0, s59
	v_lshl_add_u64 v[220:221], s[44:45], 0, v[134:135]
	global_load_lds_dwordx4 v[218:219], off
	v_lshl_add_u64 v[218:219], s[2:3], 0, v[136:137]
	s_add_i32 m0, s59, 0x2000
	s_nop 0
	global_load_lds_dwordx4 v[218:219], off
	v_lshl_add_u64 v[218:219], s[44:45], 0, v[130:131]
	s_mov_b32 m0, s9
	s_nop 0
	global_load_lds_dwordx4 v[218:219], off
	s_mov_b32 m0, s10
	s_nop 0
	global_load_lds_dwordx4 v[220:221], off
	s_waitcnt vmcnt(8)
	s_waitcnt lgkmcnt(0)
	s_barrier
	s_setprio 1
	s_waitcnt lgkmcnt(0)
	v_mfma_f32_16x16x32_bf16 v[62:65], v[144:147], v[182:185], v[62:65]
	v_mfma_f32_16x16x32_bf16 v[58:61], v[152:155], v[182:185], v[58:61]
	v_mfma_f32_16x16x32_bf16 v[46:49], v[144:147], v[190:193], v[46:49]
	v_mfma_f32_16x16x32_bf16 v[42:45], v[152:155], v[190:193], v[42:45]
	v_mfma_f32_16x16x32_bf16 v[30:33], v[144:147], v[198:201], v[30:33]
	v_mfma_f32_16x16x32_bf16 v[26:29], v[152:155], v[198:201], v[26:29]
	v_mfma_f32_16x16x32_bf16 v[14:17], v[144:147], v[206:209], v[14:17]
	v_mfma_f32_16x16x32_bf16 v[10:13], v[152:155], v[206:209], v[10:13]
	v_mfma_f32_16x16x32_bf16 v[62:65], v[148:151], v[186:189], v[62:65]
	v_mfma_f32_16x16x32_bf16 v[58:61], v[156:159], v[186:189], v[58:61]
	v_mfma_f32_16x16x32_bf16 v[46:49], v[148:151], v[194:197], v[46:49]
	v_mfma_f32_16x16x32_bf16 v[42:45], v[156:159], v[194:197], v[42:45]
	v_mfma_f32_16x16x32_bf16 v[30:33], v[148:151], v[202:205], v[30:33]
	v_mfma_f32_16x16x32_bf16 v[26:29], v[156:159], v[202:205], v[26:29]
	v_mfma_f32_16x16x32_bf16 v[14:17], v[148:151], v[210:213], v[14:17]
	v_mfma_f32_16x16x32_bf16 v[10:13], v[156:159], v[210:213], v[10:13]
	s_setprio 0
	s_setprio 1
	v_mfma_f32_16x16x32_bf16 v[54:57], v[166:169], v[182:185], v[54:57]
	v_mfma_f32_16x16x32_bf16 v[50:53], v[174:177], v[182:185], v[50:53]
	v_mfma_f32_16x16x32_bf16 v[38:41], v[166:169], v[190:193], v[38:41]
	v_mfma_f32_16x16x32_bf16 v[34:37], v[174:177], v[190:193], v[34:37]
	v_mfma_f32_16x16x32_bf16 v[22:25], v[166:169], v[198:201], v[22:25]
	v_mfma_f32_16x16x32_bf16 v[18:21], v[174:177], v[198:201], v[18:21]
	v_mfma_f32_16x16x32_bf16 v[6:9], v[166:169], v[206:209], v[6:9]
	v_mfma_f32_16x16x32_bf16 v[2:5], v[174:177], v[206:209], v[2:5]
	v_mfma_f32_16x16x32_bf16 v[54:57], v[170:173], v[186:189], v[54:57]
	v_mfma_f32_16x16x32_bf16 v[50:53], v[178:181], v[186:189], v[50:53]
	v_mfma_f32_16x16x32_bf16 v[38:41], v[170:173], v[194:197], v[38:41]
	v_mfma_f32_16x16x32_bf16 v[34:37], v[178:181], v[194:197], v[34:37]
	v_mfma_f32_16x16x32_bf16 v[22:25], v[170:173], v[202:205], v[22:25]
	v_mfma_f32_16x16x32_bf16 v[18:21], v[178:181], v[202:205], v[18:21]
	v_mfma_f32_16x16x32_bf16 v[6:9], v[170:173], v[210:213], v[6:9]
	v_mfma_f32_16x16x32_bf16 v[2:5], v[178:181], v[210:213], v[2:5]
	s_setprio 0
	s_barrier
	s_add_i32 s59, 0, 0x18000
	s_add_i32 s60, 0, 0x1c000
	v_add_u32_e32 v156, s59, v160
	v_add_u32_e32 v165, s60, v160
	ds_read_b128 v[144:147], v156
	ds_read_b128 v[148:151], v156 offset:1024
	ds_read_b128 v[152:155], v156 offset:2048
	ds_read_b128 v[156:159], v156 offset:3072
	ds_read_b128 v[166:169], v165
	ds_read_b128 v[170:173], v165 offset:1024
	ds_read_b128 v[174:177], v165 offset:2048
	ds_read_b128 v[178:181], v165 offset:3072
	s_add_u32 s2, s44, 0x80000
	s_addc_u32 s3, s45, 0
	s_mov_b32 m0, s11
	v_lshl_add_u64 v[222:223], s[2:3], 0, v[130:131]
	ds_read_b128 v[182:185], v164 offset:32768
	ds_read_b128 v[186:189], v164 offset:33792
	ds_read_b128 v[190:193], v164 offset:34816
	ds_read_b128 v[194:197], v164 offset:35840
	ds_read_b128 v[198:201], v164 offset:36864
	ds_read_b128 v[202:205], v164 offset:37888
	ds_read_b128 v[206:209], v164 offset:38912
	ds_read_b128 v[210:213], v164 offset:39936
	global_load_lds_dwordx4 v[222:223], off
	v_lshl_add_u64 v[222:223], s[2:3], 0, v[134:135]
	s_mov_b32 m0, s46
	s_nop 0
	global_load_lds_dwordx4 v[222:223], off
	s_waitcnt vmcnt(8)
	s_waitcnt lgkmcnt(0)
	s_barrier
	s_setprio 1
	s_waitcnt lgkmcnt(0)
	v_mfma_f32_16x16x32_bf16 v[126:129], v[144:147], v[182:185], v[126:129]
	v_mfma_f32_16x16x32_bf16 v[122:125], v[152:155], v[182:185], v[122:125]
	v_mfma_f32_16x16x32_bf16 v[110:113], v[144:147], v[190:193], v[110:113]
	v_mfma_f32_16x16x32_bf16 v[106:109], v[152:155], v[190:193], v[106:109]
	v_mfma_f32_16x16x32_bf16 v[94:97], v[144:147], v[198:201], v[94:97]
	v_mfma_f32_16x16x32_bf16 v[90:93], v[152:155], v[198:201], v[90:93]
	v_mfma_f32_16x16x32_bf16 v[78:81], v[144:147], v[206:209], v[78:81]
	v_mfma_f32_16x16x32_bf16 v[74:77], v[152:155], v[206:209], v[74:77]
	v_mfma_f32_16x16x32_bf16 v[126:129], v[148:151], v[186:189], v[126:129]
	v_mfma_f32_16x16x32_bf16 v[122:125], v[156:159], v[186:189], v[122:125]
	v_mfma_f32_16x16x32_bf16 v[110:113], v[148:151], v[194:197], v[110:113]
	v_mfma_f32_16x16x32_bf16 v[106:109], v[156:159], v[194:197], v[106:109]
	v_mfma_f32_16x16x32_bf16 v[94:97], v[148:151], v[202:205], v[94:97]
	v_mfma_f32_16x16x32_bf16 v[90:93], v[156:159], v[202:205], v[90:93]
	v_mfma_f32_16x16x32_bf16 v[78:81], v[148:151], v[210:213], v[78:81]
	v_mfma_f32_16x16x32_bf16 v[74:77], v[156:159], v[210:213], v[74:77]
	s_setprio 0
	s_setprio 1
	v_mfma_f32_16x16x32_bf16 v[118:121], v[166:169], v[182:185], v[118:121]
	v_mfma_f32_16x16x32_bf16 v[114:117], v[174:177], v[182:185], v[114:117]
	v_mfma_f32_16x16x32_bf16 v[102:105], v[166:169], v[190:193], v[102:105]
	v_mfma_f32_16x16x32_bf16 v[98:101], v[174:177], v[190:193], v[98:101]
	v_mfma_f32_16x16x32_bf16 v[86:89], v[166:169], v[198:201], v[86:89]
	v_mfma_f32_16x16x32_bf16 v[82:85], v[174:177], v[198:201], v[82:85]
	v_mfma_f32_16x16x32_bf16 v[70:73], v[166:169], v[206:209], v[70:73]
	v_mfma_f32_16x16x32_bf16 v[66:69], v[174:177], v[206:209], v[66:69]
	v_mfma_f32_16x16x32_bf16 v[118:121], v[170:173], v[186:189], v[118:121]
	v_mfma_f32_16x16x32_bf16 v[114:117], v[178:181], v[186:189], v[114:117]
	v_mfma_f32_16x16x32_bf16 v[102:105], v[170:173], v[194:197], v[102:105]
	v_mfma_f32_16x16x32_bf16 v[98:101], v[178:181], v[194:197], v[98:101]
	v_mfma_f32_16x16x32_bf16 v[86:89], v[170:173], v[202:205], v[86:89]
	v_mfma_f32_16x16x32_bf16 v[82:85], v[178:181], v[202:205], v[82:85]
	v_mfma_f32_16x16x32_bf16 v[70:73], v[170:173], v[210:213], v[70:73]
	v_mfma_f32_16x16x32_bf16 v[66:69], v[178:181], v[210:213], v[66:69]
	s_setprio 0
	s_barrier
	s_add_i32 s2, s59, s8
	v_lshl_add_u64 v[214:215], v[214:215], 0, s[14:15]
	s_mov_b32 m0, s2
	ds_read_b128 v[182:185], v164 offset:49152
	ds_read_b128 v[186:189], v164 offset:50176
	ds_read_b128 v[190:193], v164 offset:51200
	ds_read_b128 v[194:197], v164 offset:52224
	ds_read_b128 v[198:201], v164 offset:53248
	ds_read_b128 v[202:205], v164 offset:54272
	ds_read_b128 v[206:209], v164 offset:55296
	ds_read_b128 v[210:213], v164 offset:56320
	global_load_lds_dwordx4 v[214:215], off
	s_add_i32 m0, s2, 0x2000
	s_add_u32 s2, s42, 0x80080
	v_lshl_add_u64 v[214:215], v[216:217], 0, s[14:15]
	s_addc_u32 s3, s43, 0
	s_add_i32 s42, s60, s8
	global_load_lds_dwordx4 v[214:215], off
	v_lshl_add_u64 v[214:215], s[2:3], 0, v[132:133]
	s_mov_b32 m0, s42
	s_nop 0
	global_load_lds_dwordx4 v[214:215], off
	v_lshl_add_u64 v[214:215], s[2:3], 0, v[136:137]
	s_add_i32 m0, s42, 0x2000
	s_nop 0
	global_load_lds_dwordx4 v[214:215], off
	v_lshl_add_u64 v[214:215], v[218:219], 0, s[14:15]
	s_mov_b32 m0, s52
	s_nop 0
	global_load_lds_dwordx4 v[214:215], off
	v_lshl_add_u64 v[214:215], v[220:221], 0, s[14:15]
	s_mov_b32 m0, s53
	s_nop 0
	global_load_lds_dwordx4 v[214:215], off
	s_waitcnt vmcnt(8)
	s_waitcnt lgkmcnt(0)
	s_barrier
	s_setprio 1
	s_waitcnt lgkmcnt(0)
	v_mfma_f32_16x16x32_bf16 v[62:65], v[144:147], v[182:185], v[62:65]
	v_mfma_f32_16x16x32_bf16 v[58:61], v[152:155], v[182:185], v[58:61]
	v_mfma_f32_16x16x32_bf16 v[46:49], v[144:147], v[190:193], v[46:49]
	v_mfma_f32_16x16x32_bf16 v[42:45], v[152:155], v[190:193], v[42:45]
	v_mfma_f32_16x16x32_bf16 v[30:33], v[144:147], v[198:201], v[30:33]
	v_mfma_f32_16x16x32_bf16 v[26:29], v[152:155], v[198:201], v[26:29]
	v_mfma_f32_16x16x32_bf16 v[14:17], v[144:147], v[206:209], v[14:17]
	v_mfma_f32_16x16x32_bf16 v[10:13], v[152:155], v[206:209], v[10:13]
	v_mfma_f32_16x16x32_bf16 v[62:65], v[148:151], v[186:189], v[62:65]
	v_mfma_f32_16x16x32_bf16 v[58:61], v[156:159], v[186:189], v[58:61]
	v_mfma_f32_16x16x32_bf16 v[46:49], v[148:151], v[194:197], v[46:49]
	v_mfma_f32_16x16x32_bf16 v[42:45], v[156:159], v[194:197], v[42:45]
	v_mfma_f32_16x16x32_bf16 v[30:33], v[148:151], v[202:205], v[30:33]
	v_mfma_f32_16x16x32_bf16 v[26:29], v[156:159], v[202:205], v[26:29]
	v_mfma_f32_16x16x32_bf16 v[14:17], v[148:151], v[210:213], v[14:17]
	v_mfma_f32_16x16x32_bf16 v[10:13], v[156:159], v[210:213], v[10:13]
	s_setprio 0
	s_setprio 1
	v_mfma_f32_16x16x32_bf16 v[54:57], v[166:169], v[182:185], v[54:57]
	v_mfma_f32_16x16x32_bf16 v[50:53], v[174:177], v[182:185], v[50:53]
	v_mfma_f32_16x16x32_bf16 v[38:41], v[166:169], v[190:193], v[38:41]
	v_mfma_f32_16x16x32_bf16 v[34:37], v[174:177], v[190:193], v[34:37]
	v_mfma_f32_16x16x32_bf16 v[22:25], v[166:169], v[198:201], v[22:25]
	v_mfma_f32_16x16x32_bf16 v[18:21], v[174:177], v[198:201], v[18:21]
	v_mfma_f32_16x16x32_bf16 v[6:9], v[166:169], v[206:209], v[6:9]
	v_mfma_f32_16x16x32_bf16 v[2:5], v[174:177], v[206:209], v[2:5]
	v_mfma_f32_16x16x32_bf16 v[54:57], v[170:173], v[186:189], v[54:57]
	v_mfma_f32_16x16x32_bf16 v[50:53], v[178:181], v[186:189], v[50:53]
	v_mfma_f32_16x16x32_bf16 v[38:41], v[170:173], v[194:197], v[38:41]
	v_mfma_f32_16x16x32_bf16 v[34:37], v[178:181], v[194:197], v[34:37]
	v_mfma_f32_16x16x32_bf16 v[22:25], v[170:173], v[202:205], v[22:25]
	v_mfma_f32_16x16x32_bf16 v[18:21], v[178:181], v[202:205], v[18:21]
	v_mfma_f32_16x16x32_bf16 v[6:9], v[170:173], v[210:213], v[6:9]
	v_mfma_f32_16x16x32_bf16 v[2:5], v[178:181], v[210:213], v[2:5]
	s_setprio 0
	s_add_i32 s58, s58, 2
	s_add_u32 s56, s56, 0x100
	s_addc_u32 s57, s57, 0
	s_add_u32 s40, s40, 0x100
	s_addc_u32 s41, s41, 0
	s_cmp_gt_u32 s58, 29
	s_barrier
	s_cbranch_scc0 .LBB0_3799
	s_and_b64 vcc, exec, s[16:17]
	s_cbranch_vccz .LBB0_3802
	s_barrier

.LBB0_4375:
	ds_read_b128 v[150:153], v147
	ds_read_b128 v[154:157], v147 offset:1024
	ds_read_b128 v[158:161], v147 offset:2048
	ds_read_b128 v[162:165], v147 offset:3072
	ds_read_b128 v[166:169], v148
	ds_read_b128 v[170:173], v148 offset:1024
	ds_read_b128 v[174:177], v148 offset:2048
	ds_read_b128 v[178:181], v148 offset:3072
	s_add_u32 s2, s36, 0xfff80080
	s_addc_u32 s3, s37, -1
	s_cmp_eq_u32 s42, 28
	s_cselect_b32 s41, s10, s3
	s_cselect_b32 s40, s21, s2
	s_cselect_b32 s39, s27, s25
	s_cselect_b32 s38, s26, s23
	v_lshl_add_u64 v[142:143], s[36:37], 0, v[140:141]
	s_add_i32 m0, s35, 0xc000
	ds_read_b128 v[182:185], v149
	ds_read_b128 v[186:189], v149 offset:1024
	ds_read_b128 v[190:193], v149 offset:2048
	ds_read_b128 v[194:197], v149 offset:3072
	ds_read_b128 v[198:201], v149 offset:4096
	ds_read_b128 v[202:205], v149 offset:5120
	ds_read_b128 v[206:209], v149 offset:6144
	ds_read_b128 v[210:213], v149 offset:7168
	global_load_lds_dwordx4 v[142:143], off
	v_lshl_add_u64 v[142:143], s[36:37], 0, v[138:139]
	s_add_i32 m0, s35, 0xe000
	s_nop 0
	global_load_lds_dwordx4 v[142:143], off
	s_waitcnt vmcnt(8)
	s_waitcnt lgkmcnt(0)
	s_barrier
	s_setprio 1
	s_waitcnt lgkmcnt(0)
	v_mfma_f32_16x16x32_bf16 v[126:129], v[150:153], v[182:185], v[126:129]
	v_mfma_f32_16x16x32_bf16 v[122:125], v[158:161], v[182:185], v[122:125]
	v_mfma_f32_16x16x32_bf16 v[110:113], v[150:153], v[190:193], v[110:113]
	v_mfma_f32_16x16x32_bf16 v[106:109], v[158:161], v[190:193], v[106:109]
	v_mfma_f32_16x16x32_bf16 v[94:97], v[150:153], v[198:201], v[94:97]
	v_mfma_f32_16x16x32_bf16 v[90:93], v[158:161], v[198:201], v[90:93]
	v_mfma_f32_16x16x32_bf16 v[78:81], v[150:153], v[206:209], v[78:81]
	v_mfma_f32_16x16x32_bf16 v[74:77], v[158:161], v[206:209], v[74:77]
	v_mfma_f32_16x16x32_bf16 v[126:129], v[154:157], v[186:189], v[126:129]
	v_mfma_f32_16x16x32_bf16 v[122:125], v[162:165], v[186:189], v[122:125]
	v_mfma_f32_16x16x32_bf16 v[110:113], v[154:157], v[194:197], v[110:113]
	v_mfma_f32_16x16x32_bf16 v[106:109], v[162:165], v[194:197], v[106:109]
	v_mfma_f32_16x16x32_bf16 v[94:97], v[154:157], v[202:205], v[94:97]
	v_mfma_f32_16x16x32_bf16 v[90:93], v[162:165], v[202:205], v[90:93]
	v_mfma_f32_16x16x32_bf16 v[78:81], v[154:157], v[210:213], v[78:81]
	v_mfma_f32_16x16x32_bf16 v[74:77], v[162:165], v[210:213], v[74:77]
	s_setprio 0
	s_setprio 1
	v_mfma_f32_16x16x32_bf16 v[118:121], v[166:169], v[182:185], v[118:121]
	v_mfma_f32_16x16x32_bf16 v[114:117], v[174:177], v[182:185], v[114:117]
	v_mfma_f32_16x16x32_bf16 v[102:105], v[166:169], v[190:193], v[102:105]
	v_mfma_f32_16x16x32_bf16 v[98:101], v[174:177], v[190:193], v[98:101]
	v_mfma_f32_16x16x32_bf16 v[86:89], v[166:169], v[198:201], v[86:89]
	v_mfma_f32_16x16x32_bf16 v[82:85], v[174:177], v[198:201], v[82:85]
	v_mfma_f32_16x16x32_bf16 v[70:73], v[166:169], v[206:209], v[70:73]
	v_mfma_f32_16x16x32_bf16 v[66:69], v[174:177], v[206:209], v[66:69]
	v_mfma_f32_16x16x32_bf16 v[118:121], v[170:173], v[186:189], v[118:121]
	v_mfma_f32_16x16x32_bf16 v[114:117], v[178:181], v[186:189], v[114:117]
	v_mfma_f32_16x16x32_bf16 v[102:105], v[170:173], v[194:197], v[102:105]
	v_mfma_f32_16x16x32_bf16 v[98:101], v[178:181], v[194:197], v[98:101]
	v_mfma_f32_16x16x32_bf16 v[86:89], v[170:173], v[202:205], v[86:89]
	v_mfma_f32_16x16x32_bf16 v[82:85], v[178:181], v[202:205], v[82:85]
	v_mfma_f32_16x16x32_bf16 v[70:73], v[170:173], v[210:213], v[70:73]
	v_mfma_f32_16x16x32_bf16 v[66:69], v[178:181], v[210:213], v[66:69]
	s_setprio 0
	s_barrier
	s_add_i32 s2, s57, s31
	v_lshl_add_u64 v[142:143], s[38:39], 0, v[132:133]
	s_mov_b32 m0, s2
	ds_read_b128 v[182:185], v149 offset:16384
	ds_read_b128 v[186:189], v149 offset:17408
	ds_read_b128 v[190:193], v149 offset:18432
	ds_read_b128 v[194:197], v149 offset:19456
	ds_read_b128 v[198:201], v149 offset:20480
	ds_read_b128 v[202:205], v149 offset:21504
	ds_read_b128 v[206:209], v149 offset:22528
	ds_read_b128 v[210:213], v149 offset:23552
	global_load_lds_dwordx4 v[142:143], off
	s_add_i32 m0, s2, 0x2000
	s_add_u32 s2, s38, 0x80000
	v_lshl_add_u64 v[214:215], s[38:39], 0, v[136:137]
	s_addc_u32 s3, s39, 0
	s_add_i32 s43, s58, s31
	global_load_lds_dwordx4 v[214:215], off
	v_lshl_add_u64 v[216:217], s[2:3], 0, v[132:133]
	s_mov_b32 m0, s43
	v_lshl_add_u64 v[218:219], s[40:41], 0, v[134:135]
	global_load_lds_dwordx4 v[216:217], off
	v_lshl_add_u64 v[216:217], s[2:3], 0, v[136:137]
	s_add_i32 m0, s43, 0x2000
	s_nop 0
	global_load_lds_dwordx4 v[216:217], off
	v_lshl_add_u64 v[216:217], s[40:41], 0, v[130:131]
	s_mov_b32 m0, s35
	s_nop 0
	global_load_lds_dwordx4 v[216:217], off
	s_mov_b32 m0, s48
	s_nop 0
	global_load_lds_dwordx4 v[218:219], off
	s_waitcnt vmcnt(8)
	s_waitcnt lgkmcnt(0)
	s_barrier
	s_setprio 1
	s_waitcnt lgkmcnt(0)
	v_mfma_f32_16x16x32_bf16 v[62:65], v[150:153], v[182:185], v[62:65]
	v_mfma_f32_16x16x32_bf16 v[58:61], v[158:161], v[182:185], v[58:61]
	v_mfma_f32_16x16x32_bf16 v[46:49], v[150:153], v[190:193], v[46:49]
	v_mfma_f32_16x16x32_bf16 v[42:45], v[158:161], v[190:193], v[42:45]
	v_mfma_f32_16x16x32_bf16 v[30:33], v[150:153], v[198:201], v[30:33]
	v_mfma_f32_16x16x32_bf16 v[26:29], v[158:161], v[198:201], v[26:29]
	v_mfma_f32_16x16x32_bf16 v[14:17], v[150:153], v[206:209], v[14:17]
	v_mfma_f32_16x16x32_bf16 v[10:13], v[158:161], v[206:209], v[10:13]
	v_mfma_f32_16x16x32_bf16 v[62:65], v[154:157], v[186:189], v[62:65]
	v_mfma_f32_16x16x32_bf16 v[58:61], v[162:165], v[186:189], v[58:61]
	v_mfma_f32_16x16x32_bf16 v[46:49], v[154:157], v[194:197], v[46:49]
	v_mfma_f32_16x16x32_bf16 v[42:45], v[162:165], v[194:197], v[42:45]
	v_mfma_f32_16x16x32_bf16 v[30:33], v[154:157], v[202:205], v[30:33]
	v_mfma_f32_16x16x32_bf16 v[26:29], v[162:165], v[202:205], v[26:29]
	v_mfma_f32_16x16x32_bf16 v[14:17], v[154:157], v[210:213], v[14:17]
	v_mfma_f32_16x16x32_bf16 v[10:13], v[162:165], v[210:213], v[10:13]
	s_setprio 0
	s_setprio 1
	v_mfma_f32_16x16x32_bf16 v[54:57], v[166:169], v[182:185], v[54:57]
	v_mfma_f32_16x16x32_bf16 v[50:53], v[174:177], v[182:185], v[50:53]
	v_mfma_f32_16x16x32_bf16 v[38:41], v[166:169], v[190:193], v[38:41]
	v_mfma_f32_16x16x32_bf16 v[34:37], v[174:177], v[190:193], v[34:37]
	v_mfma_f32_16x16x32_bf16 v[22:25], v[166:169], v[198:201], v[22:25]
	v_mfma_f32_16x16x32_bf16 v[18:21], v[174:177], v[198:201], v[18:21]
	v_mfma_f32_16x16x32_bf16 v[6:9], v[166:169], v[206:209], v[6:9]
	v_mfma_f32_16x16x32_bf16 v[2:5], v[174:177], v[206:209], v[2:5]
	v_mfma_f32_16x16x32_bf16 v[54:57], v[170:173], v[186:189], v[54:57]
	v_mfma_f32_16x16x32_bf16 v[50:53], v[178:181], v[186:189], v[50:53]
	v_mfma_f32_16x16x32_bf16 v[38:41], v[170:173], v[194:197], v[38:41]
	v_mfma_f32_16x16x32_bf16 v[34:37], v[178:181], v[194:197], v[34:37]
	v_mfma_f32_16x16x32_bf16 v[22:25], v[170:173], v[202:205], v[22:25]
	v_mfma_f32_16x16x32_bf16 v[18:21], v[178:181], v[202:205], v[18:21]
	v_mfma_f32_16x16x32_bf16 v[6:9], v[170:173], v[210:213], v[6:9]
	v_mfma_f32_16x16x32_bf16 v[2:5], v[178:181], v[210:213], v[2:5]
	s_setprio 0
	s_barrier
	s_add_i32 s43, 0, 0x18000
	s_add_i32 s63, 0, 0x1c000
	v_add_u32_e32 v162, s43, v145
	v_add_u32_e32 v178, s63, v145
	ds_read_b128 v[150:153], v162
	ds_read_b128 v[154:157], v162 offset:1024
	ds_read_b128 v[158:161], v162 offset:2048
	ds_read_b128 v[162:165], v162 offset:3072
	ds_read_b128 v[166:169], v178
	ds_read_b128 v[170:173], v178 offset:1024
	ds_read_b128 v[174:177], v178 offset:2048
	ds_read_b128 v[178:181], v178 offset:3072
	s_add_u32 s2, s40, 0x80000
	s_addc_u32 s3, s41, 0
	s_mov_b32 m0, s49
	v_lshl_add_u64 v[220:221], s[2:3], 0, v[130:131]
	ds_read_b128 v[182:185], v149 offset:32768
	ds_read_b128 v[186:189], v149 offset:33792
	ds_read_b128 v[190:193], v149 offset:34816
	ds_read_b128 v[194:197], v149 offset:35840
	ds_read_b128 v[198:201], v149 offset:36864
	ds_read_b128 v[202:205], v149 offset:37888
	ds_read_b128 v[206:209], v149 offset:38912
	ds_read_b128 v[210:213], v149 offset:39936
	global_load_lds_dwordx4 v[220:221], off
	v_lshl_add_u64 v[220:221], s[2:3], 0, v[134:135]
	s_mov_b32 m0, s50
	s_nop 0
	global_load_lds_dwordx4 v[220:221], off
	s_waitcnt vmcnt(8)
	s_waitcnt lgkmcnt(0)
	s_barrier
	s_setprio 1
	s_waitcnt lgkmcnt(0)
	v_mfma_f32_16x16x32_bf16 v[126:129], v[150:153], v[182:185], v[126:129]
	v_mfma_f32_16x16x32_bf16 v[122:125], v[158:161], v[182:185], v[122:125]
	v_mfma_f32_16x16x32_bf16 v[110:113], v[150:153], v[190:193], v[110:113]
	v_mfma_f32_16x16x32_bf16 v[106:109], v[158:161], v[190:193], v[106:109]
	v_mfma_f32_16x16x32_bf16 v[94:97], v[150:153], v[198:201], v[94:97]
	v_mfma_f32_16x16x32_bf16 v[90:93], v[158:161], v[198:201], v[90:93]
	v_mfma_f32_16x16x32_bf16 v[78:81], v[150:153], v[206:209], v[78:81]
	v_mfma_f32_16x16x32_bf16 v[74:77], v[158:161], v[206:209], v[74:77]
	v_mfma_f32_16x16x32_bf16 v[126:129], v[154:157], v[186:189], v[126:129]
	v_mfma_f32_16x16x32_bf16 v[122:125], v[162:165], v[186:189], v[122:125]
	v_mfma_f32_16x16x32_bf16 v[110:113], v[154:157], v[194:197], v[110:113]
	v_mfma_f32_16x16x32_bf16 v[106:109], v[162:165], v[194:197], v[106:109]
	v_mfma_f32_16x16x32_bf16 v[94:97], v[154:157], v[202:205], v[94:97]
	v_mfma_f32_16x16x32_bf16 v[90:93], v[162:165], v[202:205], v[90:93]
	v_mfma_f32_16x16x32_bf16 v[78:81], v[154:157], v[210:213], v[78:81]
	v_mfma_f32_16x16x32_bf16 v[74:77], v[162:165], v[210:213], v[74:77]
	s_setprio 0
	s_setprio 1
	v_mfma_f32_16x16x32_bf16 v[118:121], v[166:169], v[182:185], v[118:121]
	v_mfma_f32_16x16x32_bf16 v[114:117], v[174:177], v[182:185], v[114:117]
	v_mfma_f32_16x16x32_bf16 v[102:105], v[166:169], v[190:193], v[102:105]
	v_mfma_f32_16x16x32_bf16 v[98:101], v[174:177], v[190:193], v[98:101]
	v_mfma_f32_16x16x32_bf16 v[86:89], v[166:169], v[198:201], v[86:89]
	v_mfma_f32_16x16x32_bf16 v[82:85], v[174:177], v[198:201], v[82:85]
	v_mfma_f32_16x16x32_bf16 v[70:73], v[166:169], v[206:209], v[70:73]
	v_mfma_f32_16x16x32_bf16 v[66:69], v[174:177], v[206:209], v[66:69]
	v_mfma_f32_16x16x32_bf16 v[118:121], v[170:173], v[186:189], v[118:121]
	v_mfma_f32_16x16x32_bf16 v[114:117], v[178:181], v[186:189], v[114:117]
	v_mfma_f32_16x16x32_bf16 v[102:105], v[170:173], v[194:197], v[102:105]
	v_mfma_f32_16x16x32_bf16 v[98:101], v[178:181], v[194:197], v[98:101]
	v_mfma_f32_16x16x32_bf16 v[86:89], v[170:173], v[202:205], v[86:89]
	v_mfma_f32_16x16x32_bf16 v[82:85], v[178:181], v[202:205], v[82:85]
	v_mfma_f32_16x16x32_bf16 v[70:73], v[170:173], v[210:213], v[70:73]
	v_mfma_f32_16x16x32_bf16 v[66:69], v[178:181], v[210:213], v[66:69]
	s_setprio 0
	s_barrier
	s_add_i32 s2, s43, s31
	v_lshl_add_u64 v[142:143], v[142:143], 0, s[16:17]
	s_mov_b32 m0, s2
	ds_read_b128 v[182:185], v149 offset:49152
	ds_read_b128 v[186:189], v149 offset:50176
	ds_read_b128 v[190:193], v149 offset:51200
	ds_read_b128 v[194:197], v149 offset:52224
	ds_read_b128 v[198:201], v149 offset:53248
	ds_read_b128 v[202:205], v149 offset:54272
	ds_read_b128 v[206:209], v149 offset:55296
	ds_read_b128 v[210:213], v149 offset:56320
	global_load_lds_dwordx4 v[142:143], off
	s_add_i32 m0, s2, 0x2000
	s_add_u32 s2, s38, 0x80080
	v_lshl_add_u64 v[142:143], v[214:215], 0, s[16:17]
	s_addc_u32 s3, s39, 0
	s_add_i32 s38, s63, s31
	global_load_lds_dwordx4 v[142:143], off
	v_lshl_add_u64 v[142:143], s[2:3], 0, v[132:133]
	s_mov_b32 m0, s38
	s_nop 0
	global_load_lds_dwordx4 v[142:143], off
	v_lshl_add_u64 v[142:143], s[2:3], 0, v[136:137]
	s_add_i32 m0, s38, 0x2000
	s_nop 0
	global_load_lds_dwordx4 v[142:143], off
	v_lshl_add_u64 v[142:143], v[216:217], 0, s[16:17]
	s_mov_b32 m0, s51
	s_nop 0
	global_load_lds_dwordx4 v[142:143], off
	v_lshl_add_u64 v[142:143], v[218:219], 0, s[16:17]
	s_mov_b32 m0, s52
	s_nop 0
	global_load_lds_dwordx4 v[142:143], off
	s_waitcnt vmcnt(8)
	s_waitcnt lgkmcnt(0)
	s_barrier
	s_setprio 1
	s_waitcnt lgkmcnt(0)
	v_mfma_f32_16x16x32_bf16 v[62:65], v[150:153], v[182:185], v[62:65]
	v_mfma_f32_16x16x32_bf16 v[58:61], v[158:161], v[182:185], v[58:61]
	v_mfma_f32_16x16x32_bf16 v[46:49], v[150:153], v[190:193], v[46:49]
	v_mfma_f32_16x16x32_bf16 v[42:45], v[158:161], v[190:193], v[42:45]
	v_mfma_f32_16x16x32_bf16 v[30:33], v[150:153], v[198:201], v[30:33]
	v_mfma_f32_16x16x32_bf16 v[26:29], v[158:161], v[198:201], v[26:29]
	v_mfma_f32_16x16x32_bf16 v[14:17], v[150:153], v[206:209], v[14:17]
	v_mfma_f32_16x16x32_bf16 v[10:13], v[158:161], v[206:209], v[10:13]
	v_mfma_f32_16x16x32_bf16 v[62:65], v[154:157], v[186:189], v[62:65]
	v_mfma_f32_16x16x32_bf16 v[58:61], v[162:165], v[186:189], v[58:61]
	v_mfma_f32_16x16x32_bf16 v[46:49], v[154:157], v[194:197], v[46:49]
	v_mfma_f32_16x16x32_bf16 v[42:45], v[162:165], v[194:197], v[42:45]
	v_mfma_f32_16x16x32_bf16 v[30:33], v[154:157], v[202:205], v[30:33]
	v_mfma_f32_16x16x32_bf16 v[26:29], v[162:165], v[202:205], v[26:29]
	v_mfma_f32_16x16x32_bf16 v[14:17], v[154:157], v[210:213], v[14:17]
	v_mfma_f32_16x16x32_bf16 v[10:13], v[162:165], v[210:213], v[10:13]
	s_setprio 0
	s_setprio 1
	v_mfma_f32_16x16x32_bf16 v[54:57], v[166:169], v[182:185], v[54:57]
	v_mfma_f32_16x16x32_bf16 v[50:53], v[174:177], v[182:185], v[50:53]
	v_mfma_f32_16x16x32_bf16 v[38:41], v[166:169], v[190:193], v[38:41]
	v_mfma_f32_16x16x32_bf16 v[34:37], v[174:177], v[190:193], v[34:37]
	v_mfma_f32_16x16x32_bf16 v[22:25], v[166:169], v[198:201], v[22:25]
	v_mfma_f32_16x16x32_bf16 v[18:21], v[174:177], v[198:201], v[18:21]
	v_mfma_f32_16x16x32_bf16 v[6:9], v[166:169], v[206:209], v[6:9]
	v_mfma_f32_16x16x32_bf16 v[2:5], v[174:177], v[206:209], v[2:5]
	v_mfma_f32_16x16x32_bf16 v[54:57], v[170:173], v[186:189], v[54:57]
	v_mfma_f32_16x16x32_bf16 v[50:53], v[178:181], v[186:189], v[50:53]
	v_mfma_f32_16x16x32_bf16 v[38:41], v[170:173], v[194:197], v[38:41]
	v_mfma_f32_16x16x32_bf16 v[34:37], v[178:181], v[194:197], v[34:37]
	v_mfma_f32_16x16x32_bf16 v[22:25], v[170:173], v[202:205], v[22:25]
	v_mfma_f32_16x16x32_bf16 v[18:21], v[178:181], v[202:205], v[18:21]
	v_mfma_f32_16x16x32_bf16 v[6:9], v[170:173], v[210:213], v[6:9]
	v_mfma_f32_16x16x32_bf16 v[2:5], v[178:181], v[210:213], v[2:5]
	s_setprio 0
	s_add_i32 s42, s42, 2
	s_add_u32 s23, s23, 0x100
	s_addc_u32 s25, s25, 0
	s_add_u32 s36, s36, 0x100
	s_addc_u32 s37, s37, 0
	s_cmp_gt_u32 s42, 29
	s_barrier
	s_cbranch_scc0 .LBB0_4375
	s_and_b64 vcc, exec, s[18:19]
	s_cbranch_vccz .LBB0_4378
	s_barrier

.LBB0_4559:
	ds_read_b128 v[150:153], v146
	ds_read_b128 v[154:157], v146 offset:1024
	ds_read_b128 v[158:161], v146 offset:2048
	ds_read_b128 v[162:165], v146 offset:3072
	ds_read_b128 v[166:169], v147
	ds_read_b128 v[170:173], v147 offset:1024
	ds_read_b128 v[174:177], v147 offset:2048
	ds_read_b128 v[178:181], v147 offset:3072
	s_add_u32 s2, s36, 0xfffe0080
	s_addc_u32 s38, s37, -1
	s_cmp_eq_u32 s61, 4
	s_cselect_b32 s41, s19, s38
	s_cselect_b32 s40, s58, s2
	s_cselect_b32 s39, s21, s60
	s_cselect_b32 s38, s23, s59
	v_lshl_add_u64 v[142:143], s[36:37], 0, v[140:141]
	s_add_i32 m0, s3, 0xc000
	ds_read_b128 v[182:185], v148
	ds_read_b128 v[186:189], v148 offset:1024
	ds_read_b128 v[190:193], v148 offset:2048
	ds_read_b128 v[194:197], v148 offset:3072
	ds_read_b128 v[198:201], v148 offset:4096
	ds_read_b128 v[202:205], v148 offset:5120
	ds_read_b128 v[206:209], v148 offset:6144
	ds_read_b128 v[210:213], v148 offset:7168
	global_load_lds_dwordx4 v[142:143], off
	v_lshl_add_u64 v[142:143], s[36:37], 0, v[138:139]
	s_add_i32 m0, s3, 0xe000
	s_nop 0
	global_load_lds_dwordx4 v[142:143], off
	s_waitcnt vmcnt(8)
	s_waitcnt lgkmcnt(0)
	s_barrier
	s_setprio 1
	s_waitcnt lgkmcnt(0)
	v_mfma_f32_16x16x32_bf16 v[126:129], v[150:153], v[182:185], v[126:129]
	v_mfma_f32_16x16x32_bf16 v[122:125], v[158:161], v[182:185], v[122:125]
	v_mfma_f32_16x16x32_bf16 v[118:121], v[150:153], v[190:193], v[118:121]
	v_mfma_f32_16x16x32_bf16 v[110:113], v[158:161], v[190:193], v[110:113]
	v_mfma_f32_16x16x32_bf16 v[102:105], v[150:153], v[198:201], v[102:105]
	v_mfma_f32_16x16x32_bf16 v[94:97], v[158:161], v[198:201], v[94:97]
	v_mfma_f32_16x16x32_bf16 v[86:89], v[150:153], v[206:209], v[86:89]
	v_mfma_f32_16x16x32_bf16 v[78:81], v[158:161], v[206:209], v[78:81]
	v_mfma_f32_16x16x32_bf16 v[126:129], v[154:157], v[186:189], v[126:129]
	v_mfma_f32_16x16x32_bf16 v[122:125], v[162:165], v[186:189], v[122:125]
	v_mfma_f32_16x16x32_bf16 v[118:121], v[154:157], v[194:197], v[118:121]
	v_mfma_f32_16x16x32_bf16 v[110:113], v[162:165], v[194:197], v[110:113]
	v_mfma_f32_16x16x32_bf16 v[102:105], v[154:157], v[202:205], v[102:105]
	v_mfma_f32_16x16x32_bf16 v[94:97], v[162:165], v[202:205], v[94:97]
	v_mfma_f32_16x16x32_bf16 v[86:89], v[154:157], v[210:213], v[86:89]
	v_mfma_f32_16x16x32_bf16 v[78:81], v[162:165], v[210:213], v[78:81]
	s_setprio 0
	s_setprio 1
	v_mfma_f32_16x16x32_bf16 v[114:117], v[166:169], v[182:185], v[114:117]
	v_mfma_f32_16x16x32_bf16 v[106:109], v[174:177], v[182:185], v[106:109]
	v_mfma_f32_16x16x32_bf16 v[98:101], v[166:169], v[190:193], v[98:101]
	v_mfma_f32_16x16x32_bf16 v[90:93], v[174:177], v[190:193], v[90:93]
	v_mfma_f32_16x16x32_bf16 v[82:85], v[166:169], v[198:201], v[82:85]
	v_mfma_f32_16x16x32_bf16 v[74:77], v[174:177], v[198:201], v[74:77]
	v_mfma_f32_16x16x32_bf16 v[70:73], v[166:169], v[206:209], v[70:73]
	v_mfma_f32_16x16x32_bf16 v[66:69], v[174:177], v[206:209], v[66:69]
	v_mfma_f32_16x16x32_bf16 v[114:117], v[170:173], v[186:189], v[114:117]
	v_mfma_f32_16x16x32_bf16 v[106:109], v[178:181], v[186:189], v[106:109]
	v_mfma_f32_16x16x32_bf16 v[98:101], v[170:173], v[194:197], v[98:101]
	v_mfma_f32_16x16x32_bf16 v[90:93], v[178:181], v[194:197], v[90:93]
	v_mfma_f32_16x16x32_bf16 v[82:85], v[170:173], v[202:205], v[82:85]
	v_mfma_f32_16x16x32_bf16 v[74:77], v[178:181], v[202:205], v[74:77]
	v_mfma_f32_16x16x32_bf16 v[70:73], v[170:173], v[210:213], v[70:73]
	v_mfma_f32_16x16x32_bf16 v[66:69], v[178:181], v[210:213], v[66:69]
	s_setprio 0
	s_barrier
	s_add_i32 s2, s52, s47
	v_lshl_add_u64 v[142:143], s[38:39], 0, v[134:135]
	s_mov_b32 m0, s2
	ds_read_b128 v[182:185], v148 offset:16384
	ds_read_b128 v[186:189], v148 offset:17408
	ds_read_b128 v[190:193], v148 offset:18432
	ds_read_b128 v[194:197], v148 offset:19456
	ds_read_b128 v[198:201], v148 offset:20480
	ds_read_b128 v[202:205], v148 offset:21504
	ds_read_b128 v[206:209], v148 offset:22528
	ds_read_b128 v[210:213], v148 offset:23552
	global_load_lds_dwordx4 v[142:143], off
	s_add_i32 m0, s2, 0x2000
	s_add_u32 s62, s38, 0x20000
	v_lshl_add_u64 v[214:215], s[38:39], 0, v[130:131]
	s_addc_u32 s63, s39, 0
	s_add_i32 s2, s53, s47
	global_load_lds_dwordx4 v[214:215], off
	v_lshl_add_u64 v[216:217], s[62:63], 0, v[134:135]
	s_mov_b32 m0, s2
	v_lshl_add_u64 v[218:219], s[40:41], 0, v[132:133]
	global_load_lds_dwordx4 v[216:217], off
	v_lshl_add_u64 v[216:217], s[62:63], 0, v[130:131]
	s_add_i32 m0, s2, 0x2000
	s_nop 0
	global_load_lds_dwordx4 v[216:217], off
	v_lshl_add_u64 v[216:217], s[40:41], 0, v[136:137]
	s_mov_b32 m0, s3
	s_nop 0
	global_load_lds_dwordx4 v[216:217], off
	s_mov_b32 m0, s31
	s_nop 0
	global_load_lds_dwordx4 v[218:219], off
	s_waitcnt vmcnt(8)
	s_waitcnt lgkmcnt(0)
	s_barrier
	s_setprio 1
	s_waitcnt lgkmcnt(0)
	v_mfma_f32_16x16x32_bf16 v[62:65], v[150:153], v[182:185], v[62:65]
	v_mfma_f32_16x16x32_bf16 v[58:61], v[158:161], v[182:185], v[58:61]
	v_mfma_f32_16x16x32_bf16 v[54:57], v[150:153], v[190:193], v[54:57]
	v_mfma_f32_16x16x32_bf16 v[46:49], v[158:161], v[190:193], v[46:49]
	v_mfma_f32_16x16x32_bf16 v[38:41], v[150:153], v[198:201], v[38:41]
	v_mfma_f32_16x16x32_bf16 v[30:33], v[158:161], v[198:201], v[30:33]
	v_mfma_f32_16x16x32_bf16 v[22:25], v[150:153], v[206:209], v[22:25]
	v_mfma_f32_16x16x32_bf16 v[14:17], v[158:161], v[206:209], v[14:17]
	v_mfma_f32_16x16x32_bf16 v[62:65], v[154:157], v[186:189], v[62:65]
	v_mfma_f32_16x16x32_bf16 v[58:61], v[162:165], v[186:189], v[58:61]
	v_mfma_f32_16x16x32_bf16 v[54:57], v[154:157], v[194:197], v[54:57]
	v_mfma_f32_16x16x32_bf16 v[46:49], v[162:165], v[194:197], v[46:49]
	v_mfma_f32_16x16x32_bf16 v[38:41], v[154:157], v[202:205], v[38:41]
	v_mfma_f32_16x16x32_bf16 v[30:33], v[162:165], v[202:205], v[30:33]
	v_mfma_f32_16x16x32_bf16 v[22:25], v[154:157], v[210:213], v[22:25]
	v_mfma_f32_16x16x32_bf16 v[14:17], v[162:165], v[210:213], v[14:17]
	s_setprio 0
	s_setprio 1
	v_mfma_f32_16x16x32_bf16 v[50:53], v[166:169], v[182:185], v[50:53]
	v_mfma_f32_16x16x32_bf16 v[42:45], v[174:177], v[182:185], v[42:45]
	v_mfma_f32_16x16x32_bf16 v[34:37], v[166:169], v[190:193], v[34:37]
	v_mfma_f32_16x16x32_bf16 v[26:29], v[174:177], v[190:193], v[26:29]
	v_mfma_f32_16x16x32_bf16 v[18:21], v[166:169], v[198:201], v[18:21]
	v_mfma_f32_16x16x32_bf16 v[10:13], v[174:177], v[198:201], v[10:13]
	v_mfma_f32_16x16x32_bf16 v[6:9], v[166:169], v[206:209], v[6:9]
	v_mfma_f32_16x16x32_bf16 v[2:5], v[174:177], v[206:209], v[2:5]
	v_mfma_f32_16x16x32_bf16 v[50:53], v[170:173], v[186:189], v[50:53]
	v_mfma_f32_16x16x32_bf16 v[42:45], v[178:181], v[186:189], v[42:45]
	v_mfma_f32_16x16x32_bf16 v[34:37], v[170:173], v[194:197], v[34:37]
	v_mfma_f32_16x16x32_bf16 v[26:29], v[178:181], v[194:197], v[26:29]
	v_mfma_f32_16x16x32_bf16 v[18:21], v[170:173], v[202:205], v[18:21]
	v_mfma_f32_16x16x32_bf16 v[10:13], v[178:181], v[202:205], v[10:13]
	v_mfma_f32_16x16x32_bf16 v[6:9], v[170:173], v[210:213], v[6:9]
	v_mfma_f32_16x16x32_bf16 v[2:5], v[178:181], v[210:213], v[2:5]
	s_setprio 0
	s_barrier
	s_add_i32 s2, 0, 0x18000
	v_add_u32_e32 v149, s2, v144
	s_add_i32 s62, 0, 0x1c000
	ds_read_b128 v[150:153], v149
	ds_read_b128 v[154:157], v149 offset:1024
	ds_read_b128 v[158:161], v149 offset:2048
	ds_read_b128 v[162:165], v149 offset:3072
	v_add_u32_e32 v149, s62, v144
	ds_read_b128 v[166:169], v149
	ds_read_b128 v[170:173], v149 offset:1024
	ds_read_b128 v[174:177], v149 offset:2048
	ds_read_b128 v[178:181], v149 offset:3072
	s_add_u32 s40, s40, 0x20000
	s_addc_u32 s41, s41, 0
	s_mov_b32 m0, s35
	v_lshl_add_u64 v[220:221], s[40:41], 0, v[136:137]
	ds_read_b128 v[182:185], v148 offset:32768
	ds_read_b128 v[186:189], v148 offset:33792
	ds_read_b128 v[190:193], v148 offset:34816
	ds_read_b128 v[194:197], v148 offset:35840
	ds_read_b128 v[198:201], v148 offset:36864
	ds_read_b128 v[202:205], v148 offset:37888
	ds_read_b128 v[206:209], v148 offset:38912
	ds_read_b128 v[210:213], v148 offset:39936
	global_load_lds_dwordx4 v[220:221], off
	v_lshl_add_u64 v[220:221], s[40:41], 0, v[132:133]
	s_mov_b32 m0, s48
	s_nop 0
	global_load_lds_dwordx4 v[220:221], off
	s_waitcnt vmcnt(8)
	s_waitcnt lgkmcnt(0)
	s_barrier
	s_setprio 1
	s_waitcnt lgkmcnt(0)
	v_mfma_f32_16x16x32_bf16 v[126:129], v[150:153], v[182:185], v[126:129]
	v_mfma_f32_16x16x32_bf16 v[122:125], v[158:161], v[182:185], v[122:125]
	v_mfma_f32_16x16x32_bf16 v[118:121], v[150:153], v[190:193], v[118:121]
	v_mfma_f32_16x16x32_bf16 v[110:113], v[158:161], v[190:193], v[110:113]
	v_mfma_f32_16x16x32_bf16 v[102:105], v[150:153], v[198:201], v[102:105]
	v_mfma_f32_16x16x32_bf16 v[94:97], v[158:161], v[198:201], v[94:97]
	v_mfma_f32_16x16x32_bf16 v[86:89], v[150:153], v[206:209], v[86:89]
	v_mfma_f32_16x16x32_bf16 v[78:81], v[158:161], v[206:209], v[78:81]
	v_mfma_f32_16x16x32_bf16 v[126:129], v[154:157], v[186:189], v[126:129]
	v_mfma_f32_16x16x32_bf16 v[122:125], v[162:165], v[186:189], v[122:125]
	v_mfma_f32_16x16x32_bf16 v[118:121], v[154:157], v[194:197], v[118:121]
	v_mfma_f32_16x16x32_bf16 v[110:113], v[162:165], v[194:197], v[110:113]
	v_mfma_f32_16x16x32_bf16 v[102:105], v[154:157], v[202:205], v[102:105]
	v_mfma_f32_16x16x32_bf16 v[94:97], v[162:165], v[202:205], v[94:97]
	v_mfma_f32_16x16x32_bf16 v[86:89], v[154:157], v[210:213], v[86:89]
	v_mfma_f32_16x16x32_bf16 v[78:81], v[162:165], v[210:213], v[78:81]
	s_setprio 0
	s_setprio 1
	v_mfma_f32_16x16x32_bf16 v[114:117], v[166:169], v[182:185], v[114:117]
	v_mfma_f32_16x16x32_bf16 v[106:109], v[174:177], v[182:185], v[106:109]
	v_mfma_f32_16x16x32_bf16 v[98:101], v[166:169], v[190:193], v[98:101]
	v_mfma_f32_16x16x32_bf16 v[90:93], v[174:177], v[190:193], v[90:93]
	v_mfma_f32_16x16x32_bf16 v[82:85], v[166:169], v[198:201], v[82:85]
	v_mfma_f32_16x16x32_bf16 v[74:77], v[174:177], v[198:201], v[74:77]
	v_mfma_f32_16x16x32_bf16 v[70:73], v[166:169], v[206:209], v[70:73]
	v_mfma_f32_16x16x32_bf16 v[66:69], v[174:177], v[206:209], v[66:69]
	v_mfma_f32_16x16x32_bf16 v[114:117], v[170:173], v[186:189], v[114:117]
	v_mfma_f32_16x16x32_bf16 v[106:109], v[178:181], v[186:189], v[106:109]
	v_mfma_f32_16x16x32_bf16 v[98:101], v[170:173], v[194:197], v[98:101]
	v_mfma_f32_16x16x32_bf16 v[90:93], v[178:181], v[194:197], v[90:93]
	v_mfma_f32_16x16x32_bf16 v[82:85], v[170:173], v[202:205], v[82:85]
	v_mfma_f32_16x16x32_bf16 v[74:77], v[178:181], v[202:205], v[74:77]
	v_mfma_f32_16x16x32_bf16 v[70:73], v[170:173], v[210:213], v[70:73]
	v_mfma_f32_16x16x32_bf16 v[66:69], v[178:181], v[210:213], v[66:69]
	s_setprio 0
	s_barrier
	s_add_i32 s2, s2, s47
	v_lshl_add_u64 v[142:143], v[142:143], 0, s[6:7]
	s_mov_b32 m0, s2
	ds_read_b128 v[182:185], v148 offset:49152
	ds_read_b128 v[186:189], v148 offset:50176
	ds_read_b128 v[190:193], v148 offset:51200
	ds_read_b128 v[194:197], v148 offset:52224
	ds_read_b128 v[198:201], v148 offset:53248
	ds_read_b128 v[202:205], v148 offset:54272
	ds_read_b128 v[206:209], v148 offset:55296
	ds_read_b128 v[210:213], v148 offset:56320
	global_load_lds_dwordx4 v[142:143], off
	s_add_i32 m0, s2, 0x2000
	s_add_u32 s38, s38, 0x20080
	v_lshl_add_u64 v[142:143], v[214:215], 0, s[6:7]
	s_addc_u32 s39, s39, 0
	s_add_i32 s2, s62, s47
	global_load_lds_dwordx4 v[142:143], off
	v_lshl_add_u64 v[142:143], s[38:39], 0, v[134:135]
	s_mov_b32 m0, s2
	s_nop 0
	global_load_lds_dwordx4 v[142:143], off
	v_lshl_add_u64 v[142:143], s[38:39], 0, v[130:131]
	s_add_i32 m0, s2, 0x2000
	s_nop 0
	global_load_lds_dwordx4 v[142:143], off
	v_lshl_add_u64 v[142:143], v[216:217], 0, s[6:7]
	s_mov_b32 m0, s49
	s_nop 0
	global_load_lds_dwordx4 v[142:143], off
	v_lshl_add_u64 v[142:143], v[218:219], 0, s[6:7]
	s_mov_b32 m0, s50
	s_nop 0
	global_load_lds_dwordx4 v[142:143], off
	s_waitcnt vmcnt(8)
	s_waitcnt lgkmcnt(0)
	s_barrier
	s_setprio 1
	s_waitcnt lgkmcnt(0)
	v_mfma_f32_16x16x32_bf16 v[62:65], v[150:153], v[182:185], v[62:65]
	v_mfma_f32_16x16x32_bf16 v[58:61], v[158:161], v[182:185], v[58:61]
	v_mfma_f32_16x16x32_bf16 v[54:57], v[150:153], v[190:193], v[54:57]
	v_mfma_f32_16x16x32_bf16 v[46:49], v[158:161], v[190:193], v[46:49]
	v_mfma_f32_16x16x32_bf16 v[38:41], v[150:153], v[198:201], v[38:41]
	v_mfma_f32_16x16x32_bf16 v[30:33], v[158:161], v[198:201], v[30:33]
	v_mfma_f32_16x16x32_bf16 v[22:25], v[150:153], v[206:209], v[22:25]
	v_mfma_f32_16x16x32_bf16 v[14:17], v[158:161], v[206:209], v[14:17]
	v_mfma_f32_16x16x32_bf16 v[62:65], v[154:157], v[186:189], v[62:65]
	v_mfma_f32_16x16x32_bf16 v[58:61], v[162:165], v[186:189], v[58:61]
	v_mfma_f32_16x16x32_bf16 v[54:57], v[154:157], v[194:197], v[54:57]
	v_mfma_f32_16x16x32_bf16 v[46:49], v[162:165], v[194:197], v[46:49]
	v_mfma_f32_16x16x32_bf16 v[38:41], v[154:157], v[202:205], v[38:41]
	v_mfma_f32_16x16x32_bf16 v[30:33], v[162:165], v[202:205], v[30:33]
	v_mfma_f32_16x16x32_bf16 v[22:25], v[154:157], v[210:213], v[22:25]
	v_mfma_f32_16x16x32_bf16 v[14:17], v[162:165], v[210:213], v[14:17]
	s_setprio 0
	s_setprio 1
	v_mfma_f32_16x16x32_bf16 v[50:53], v[166:169], v[182:185], v[50:53]
	v_mfma_f32_16x16x32_bf16 v[42:45], v[174:177], v[182:185], v[42:45]
	v_mfma_f32_16x16x32_bf16 v[34:37], v[166:169], v[190:193], v[34:37]
	v_mfma_f32_16x16x32_bf16 v[26:29], v[174:177], v[190:193], v[26:29]
	v_mfma_f32_16x16x32_bf16 v[18:21], v[166:169], v[198:201], v[18:21]
	v_mfma_f32_16x16x32_bf16 v[10:13], v[174:177], v[198:201], v[10:13]
	v_mfma_f32_16x16x32_bf16 v[6:9], v[166:169], v[206:209], v[6:9]
	v_mfma_f32_16x16x32_bf16 v[2:5], v[174:177], v[206:209], v[2:5]
	v_mfma_f32_16x16x32_bf16 v[50:53], v[170:173], v[186:189], v[50:53]
	v_mfma_f32_16x16x32_bf16 v[42:45], v[178:181], v[186:189], v[42:45]
	v_mfma_f32_16x16x32_bf16 v[34:37], v[170:173], v[194:197], v[34:37]
	v_mfma_f32_16x16x32_bf16 v[26:29], v[178:181], v[194:197], v[26:29]
	v_mfma_f32_16x16x32_bf16 v[18:21], v[170:173], v[202:205], v[18:21]
	v_mfma_f32_16x16x32_bf16 v[10:13], v[178:181], v[202:205], v[10:13]
	v_mfma_f32_16x16x32_bf16 v[6:9], v[170:173], v[210:213], v[6:9]
	v_mfma_f32_16x16x32_bf16 v[2:5], v[178:181], v[210:213], v[2:5]
	s_setprio 0
	s_add_i32 s61, s61, 2
	s_add_u32 s59, s59, 0x100
	s_addc_u32 s60, s60, 0
	s_add_u32 s36, s36, 0x100
	s_addc_u32 s37, s37, 0
	s_cmp_gt_u32 s61, 5
	s_barrier
	s_cbranch_scc0 .LBB0_4559
	s_and_b64 vcc, exec, s[8:9]
	s_cbranch_vccz .LBB0_4562
	s_barrier
